# k0 K-kind epilogue: forward/backward transposed-copy dwordx2 store pairs merged into one dwordx4 store via v_permlane16_swap (64 -> 32 stores per wave)
# speedup vs baseline: 1.0062x; 1.0062x over previous
.LBB0_319:
	v_bfe_u32 v202, v249, 4, 1
	v_mul_u32_u24_e32 v202, 0x3fff8, v202
	v_mov_b32_e32 v203, 0
	s_add_u32 s40, s58, 0x1ea00000
	s_addc_u32 s41, s59, 0
	s_cmp_lg_u32 s45, 0
	s_cselect_b64 s[34:35], -1, 0
	s_ashr_i32 s45, s44, 31
	s_lshl_b64 s[8:9], s[44:45], 2
	s_add_u32 s36, s94, s8
	s_addc_u32 s37, s95, s9
	global_load_dword v66, v67, s[36:37]
	global_load_dword v140, v67, s[36:37] offset:16
	s_mov_b32 s8, 0xbfb8aa3b
	s_mov_b32 s11, 0x3f317218
	v_mov_b32_e32 v168, 0x3ecc95a3
	s_mov_b32 s10, 0x7f800000
	s_mov_b32 s12, 0x33800000
	s_add_i32 s7, s7, s93
	v_mov_b32_e32 v248, 0x3ecc95a3
	s_waitcnt vmcnt(0)
	v_mul_f32_e32 v141, 0xbfb8aa3b, v66
	v_mul_f32_e32 v142, 0xbfb8aa3b, v140
	v_fma_f32 v143, v66, s8, -v141
	v_rndne_f32_e32 v144, v141
	v_fma_f32 v145, v140, s8, -v142
	v_rndne_f32_e32 v146, v142
	v_fmac_f32_e32 v143, 0xb2a5705f, v66
	v_sub_f32_e32 v141, v141, v144
	v_fmac_f32_e32 v145, 0xb2a5705f, v140
	v_sub_f32_e32 v142, v142, v146
	v_add_f32_e32 v141, v141, v143
	v_cvt_i32_f32_e32 v144, v144
	v_add_f32_e32 v142, v142, v145
	v_exp_f32_e32 v141, v141
	v_cvt_i32_f32_e32 v146, v146
	v_exp_f32_e32 v142, v142
	s_mov_b32 s8, 0x42ce8ed0
	v_ldexp_f32 v141, v141, v144
	v_cmp_nlt_f32_e32 vcc, s8, v66
	v_ldexp_f32 v142, v142, v146
	s_nop 0
	v_cndmask_b32_e32 v141, 0, v141, vcc
	v_cmp_nlt_f32_e32 vcc, s8, v140
	s_mov_b32 s8, 0xc2b17218
	s_nop 0
	v_cndmask_b32_e32 v142, 0, v142, vcc
	v_cmp_ngt_f32_e32 vcc, s8, v66
	s_nop 1
	v_cndmask_b32_e32 v66, v252, v141, vcc
	v_cmp_ngt_f32_e32 vcc, s8, v140
	v_add_f32_e32 v144, 1.0, v66
	v_frexp_mant_f32_e32 v147, v144
	v_cndmask_b32_e32 v156, v252, v142, vcc
	v_cvt_f64_f32_e32 v[140:141], v144
	s_mov_b32 s8, 0x3f2aaaab
	v_add_f32_e32 v145, 1.0, v156
	v_add_f32_e32 v146, -1.0, v144
	v_frexp_exp_i32_f64_e32 v140, v[140:141]
	v_cmp_gt_f32_e32 vcc, s8, v147
	v_add_f32_e32 v148, -1.0, v145
	v_frexp_mant_f32_e32 v149, v145
	v_cvt_f64_f32_e32 v[142:143], v145
	v_sub_f32_e32 v150, v146, v144
	v_subbrev_co_u32_e32 v140, vcc, 0, v140, vcc
	v_sub_f32_e32 v146, v66, v146
	v_sub_f32_e32 v141, v148, v145
	v_frexp_exp_i32_f64_e32 v142, v[142:143]
	v_add_f32_e32 v143, 1.0, v150
	v_cmp_gt_f32_e32 vcc, s8, v149
	v_sub_f32_e32 v148, v156, v148
	v_add_f32_e32 v141, 1.0, v141
	v_subbrev_co_u32_e32 v157, vcc, 0, v142, vcc
	v_add_f32_e32 v142, v146, v143
	v_sub_u32_e32 v143, 0, v140
	v_cvt_f32_i32_e32 v140, v140
	v_add_f32_e32 v141, v148, v141
	v_sub_u32_e32 v146, 0, v157
	v_ldexp_f32 v144, v144, v143
	v_ldexp_f32 v142, v142, v143
	v_ldexp_f32 v143, v145, v146
	v_ldexp_f32 v141, v141, v146
	v_add_f32_e32 v145, -1.0, v144
	v_add_f32_e32 v146, 1.0, v144
	v_add_f32_e32 v147, 1.0, v145
	v_add_f32_e32 v148, -1.0, v146
	v_sub_f32_e32 v147, v144, v147
	v_sub_f32_e32 v144, v144, v148
	v_mul_f32_e32 v148, 0x3f317218, v140
	v_add_f32_e32 v147, v142, v147
	v_add_f32_e32 v142, v142, v144
	v_fma_f32 v144, v140, s11, -v148
	v_add_f32_e32 v149, v145, v147
	v_add_f32_e32 v150, v146, v142
	v_fmac_f32_e32 v144, 0xb102e308, v140
	v_sub_f32_e32 v140, v145, v149
	v_sub_f32_e32 v145, v146, v150
	v_rcp_f32_e32 v146, v150
	v_add_f32_e32 v151, v148, v144
	v_add_f32_e32 v142, v142, v145
	v_sub_f32_e32 v145, v151, v148
	v_sub_f32_e32 v144, v144, v145
	v_mul_f32_e32 v145, v149, v146
	v_add_f32_e32 v140, v147, v140
	v_mul_f32_e32 v147, v150, v145
	v_fma_f32 v148, v145, v150, -v147
	v_fmac_f32_e32 v148, v145, v142
	v_add_f32_e32 v152, v147, v148
	v_sub_f32_e32 v153, v149, v152
	v_sub_f32_e32 v147, v152, v147
	v_sub_f32_e32 v149, v149, v153
	v_sub_f32_e32 v147, v147, v148
	v_sub_f32_e32 v148, v149, v152
	v_add_f32_e32 v140, v140, v148
	v_add_f32_e32 v140, v147, v140
	v_add_f32_e32 v147, v153, v140
	v_mul_f32_e32 v148, v146, v147
	v_sub_f32_e32 v149, v153, v147
	v_mul_f32_e32 v152, v150, v148
	v_add_f32_e32 v140, v140, v149
	v_add_f32_e32 v149, v145, v148
	v_fma_f32 v150, v148, v150, -v152
	v_sub_f32_e32 v145, v149, v145
	v_fmac_f32_e32 v150, v148, v142
	v_sub_f32_e32 v142, v148, v145
	v_add_f32_e32 v145, v152, v150
	v_sub_f32_e32 v148, v145, v152
	v_sub_f32_e32 v152, v147, v145
	v_sub_f32_e32 v147, v147, v152
	v_sub_f32_e32 v145, v147, v145
	v_sub_f32_e32 v148, v148, v150
	v_add_f32_e32 v140, v140, v145
	v_add_f32_e32 v140, v148, v140
	v_add_f32_e32 v140, v152, v140
	v_mul_f32_e32 v140, v146, v140
	v_add_f32_e32 v140, v142, v140
	v_add_f32_e32 v142, v149, v140
	v_mul_f32_e32 v145, v142, v142
	v_fmamk_f32 v148, v145, 0x3e9b6dac, v168
	v_sub_f32_e32 v146, v142, v149
	v_ldexp_f32 v147, v142, 1
	v_mul_f32_e32 v142, v142, v145
	v_fmaak_f32 v145, v145, v148, 0x3f2aaada
	v_mul_f32_e32 v142, v142, v145
	v_add_f32_e32 v145, v147, v142
	v_sub_f32_e32 v140, v140, v146
	v_sub_f32_e32 v146, v145, v147
	v_ldexp_f32 v140, v140, 1
	v_sub_f32_e32 v142, v142, v146
	v_add_f32_e32 v140, v140, v142
	v_add_f32_e32 v142, v145, v140
	v_sub_f32_e32 v145, v142, v145
	v_add_f32_e32 v146, v151, v142
	v_sub_f32_e32 v140, v140, v145
	v_sub_f32_e32 v145, v146, v151
	v_sub_f32_e32 v147, v146, v145
	v_sub_f32_e32 v142, v142, v145
	v_add_f32_e32 v145, v144, v140
	v_sub_f32_e32 v147, v151, v147
	v_sub_f32_e32 v148, v145, v144
	v_add_f32_e32 v142, v142, v147
	v_sub_f32_e32 v147, v145, v148
	v_sub_f32_e32 v140, v140, v148
	v_sub_f32_e32 v144, v144, v147
	v_add_f32_e32 v142, v145, v142
	v_add_f32_e32 v140, v140, v144
	v_add_f32_e32 v144, v146, v142
	v_sub_f32_e32 v145, v144, v146
	v_sub_f32_e32 v142, v142, v145
	v_add_f32_e32 v140, v140, v142
	v_add_f32_e32 v140, v144, v140
	v_cmp_neq_f32_e32 vcc, s10, v66
	v_add_f32_e32 v144, 1.0, v143
	v_add_f32_e32 v145, -1.0, v144
	v_cndmask_b32_e32 v140, v252, v140, vcc
	v_cmp_lt_f32_e64 vcc, |v66|, s12
	s_mov_b32 s8, 0x200000
	v_cvt_f32_i32_e32 v157, v157
	v_cndmask_b32_e32 v158, v140, v66, vcc
	v_add_f32_e32 v66, -1.0, v143
	v_add_f32_e32 v140, 1.0, v66
	v_sub_f32_e32 v140, v143, v140
	v_sub_f32_e32 v143, v143, v145
	v_add_f32_e32 v140, v141, v140
	v_add_f32_e32 v141, v141, v143
	v_add_f32_e32 v143, v144, v141
	v_rcp_f32_e32 v159, v143
	v_add_f32_e32 v142, v66, v140
	v_sub_f32_e32 v66, v66, v142
	v_add_f32_e32 v66, v140, v66
	v_sub_f32_e32 v140, v144, v143
	v_mul_f32_e32 v160, v142, v159
	v_add_f32_e32 v140, v141, v140
	v_mul_f32_e32 v141, v143, v160
	v_fma_f32 v144, v160, v143, -v141
	v_fmac_f32_e32 v144, v160, v140
	v_add_f32_e32 v145, v141, v144
	v_sub_f32_e32 v146, v142, v145
	v_sub_f32_e32 v142, v142, v146
	v_sub_f32_e32 v141, v145, v141
	v_sub_f32_e32 v142, v142, v145
	v_add_f32_e32 v66, v66, v142
	v_sub_f32_e32 v141, v141, v144
	v_add_f32_e32 v66, v141, v66
	v_add_f32_e32 v161, v146, v66
	v_mul_f32_e32 v162, v159, v161
	v_mul_f32_e32 v141, v143, v162
	v_fma_f32 v163, v162, v143, -v141
	v_fmac_f32_e32 v163, v162, v140
	v_sub_f32_e32 v140, v146, v161
	v_add_f32_e32 v164, v66, v140
	v_lshlrev_b32_e32 v66, 2, v216
	v_lshl_add_u64 v[152:153], s[58:59], 0, v[66:67]
	v_add_co_u32_e32 v144, vcc, s8, v152
	s_mov_b64 s[8:9], 0x200000
	v_add_f32_e32 v165, v141, v163
	v_addc_co_u32_e32 v145, vcc, 0, v153, vcc
	v_lshl_add_u64 v[148:149], v[152:153], 0, s[8:9]
	v_sub_f32_e32 v166, v165, v141
	global_load_dwordx4 v[140:143], v[144:145], off
	s_nop 0
	global_load_dwordx4 v[144:147], v[144:145], off offset:512
	s_nop 0
	global_load_dwordx4 v[148:151], v[148:149], off offset:16
	s_mov_b64 s[8:9], 0x200200
	v_lshl_add_u64 v[152:153], v[152:153], 0, s[8:9]
	global_load_dwordx4 v[152:155], v[152:153], off offset:16
	v_sub_f32_e32 v167, v161, v165
	v_sub_f32_e32 v66, v161, v167
	v_sub_f32_e32 v66, v66, v165
	v_add_f32_e32 v66, v164, v66
	v_sub_f32_e32 v161, v166, v163
	v_add_f32_e32 v66, v161, v66
	v_add_f32_e32 v66, v167, v66
	v_mul_f32_e32 v66, v159, v66
	v_add_f32_e32 v159, v160, v162
	v_sub_f32_e32 v160, v159, v160
	v_sub_f32_e32 v160, v162, v160
	v_add_f32_e32 v66, v160, v66
	v_mul_f32_e32 v163, 0x3f317218, v157
	v_add_f32_e32 v160, v159, v66
	v_fma_f32 v164, v157, s11, -v163
	v_mul_f32_e32 v161, v160, v160
	v_fmac_f32_e32 v164, 0xb102e308, v157
	v_sub_f32_e32 v157, v160, v159
	v_fmamk_f32 v162, v161, 0x3e9b6dac, v168
	v_sub_f32_e32 v66, v66, v157
	v_add_f32_e32 v157, v163, v164
	v_fmaak_f32 v162, v161, v162, 0x3f2aaada
	v_sub_f32_e32 v159, v157, v163
	v_ldexp_f32 v163, v160, 1
	v_mul_f32_e32 v160, v160, v161
	v_mul_f32_e32 v160, v160, v162
	v_add_f32_e32 v161, v163, v160
	v_sub_f32_e32 v162, v161, v163
	v_ldexp_f32 v66, v66, 1
	v_sub_f32_e32 v160, v160, v162
	v_add_f32_e32 v66, v66, v160
	v_add_f32_e32 v160, v161, v66
	v_sub_f32_e32 v161, v160, v161
	v_sub_f32_e32 v66, v66, v161
	v_add_f32_e32 v161, v157, v160
	v_sub_f32_e32 v162, v161, v157
	v_sub_f32_e32 v163, v161, v162
	v_sub_f32_e32 v159, v164, v159
	v_sub_f32_e32 v157, v157, v163
	v_sub_f32_e32 v160, v160, v162
	v_add_f32_e32 v157, v160, v157
	v_add_f32_e32 v160, v159, v66
	v_sub_f32_e32 v162, v160, v159
	v_sub_f32_e32 v163, v160, v162
	v_sub_f32_e32 v159, v159, v163
	v_sub_f32_e32 v66, v66, v162
	v_add_f32_e32 v157, v160, v157
	v_add_f32_e32 v66, v66, v159
	v_add_f32_e32 v159, v161, v157
	v_sub_f32_e32 v160, v159, v161
	v_sub_f32_e32 v157, v157, v160
	v_add_f32_e32 v66, v66, v157
	v_mul_f32_e32 v171, 0xbfb8aa3b, v158
	v_add_u32_e32 v158, s7, v205
	v_add_f32_e32 v66, v159, v66
	v_and_b32_e32 v159, 0xfff, v158
	v_cvt_f32_u32_e32 v159, v159
	s_lshl_b32 s8, s44, 8
	v_cmp_neq_f32_e32 vcc, s10, v156
	s_ashr_i32 s9, s8, 31
	s_lshl_b64 s[8:9], s[8:9], 1
	v_cndmask_b32_e32 v66, v252, v66, vcc
	v_cmp_lt_f32_e64 vcc, |v156|, s12
	s_add_u32 s8, s58, s8
	s_addc_u32 s9, s59, s9
	v_cndmask_b32_e32 v66, v66, v156, vcc
	v_mul_f32_e32 v170, 0xbfb8aa3b, v66
	v_lshlrev_b32_e32 v66, 1, v216
	v_lshl_add_u64 v[168:169], s[8:9], 0, v[66:67]
	s_mov_b64 s[8:9], 0xca00000
	v_lshl_add_u64 v[156:157], v[168:169], 0, s[8:9]
	s_lshl_b64 s[8:9], s[44:45], 11
	s_add_u32 s58, s58, s8
	s_addc_u32 s59, s59, s9
	s_and_b64 vcc, exec, s[34:35]
	s_waitcnt vmcnt(3)
	v_mul_f32_e32 v160, v140, v159
	s_waitcnt vmcnt(1)
	v_mul_f32_e32 v161, v148, v159
	v_fract_f32_e32 v160, v160
	v_fract_f32_e32 v161, v161
	v_fmac_f32_e32 v160, v159, v144
	s_waitcnt vmcnt(0)
	v_fmac_f32_e32 v161, v159, v152
	v_cos_f32_e32 v172, v160
	v_sin_f32_e32 v174, v160
	v_cos_f32_e32 v176, v161
	v_sin_f32_e32 v178, v161
	v_mul_f32_e32 v160, v141, v159
	v_mul_f32_e32 v161, v149, v159
	v_fract_f32_e32 v160, v160
	v_fract_f32_e32 v161, v161
	v_fmac_f32_e32 v160, v159, v145
	v_fmac_f32_e32 v161, v159, v153
	v_cos_f32_e32 v173, v160
	v_sin_f32_e32 v175, v160
	v_cos_f32_e32 v177, v161
	v_sin_f32_e32 v179, v161
	v_mul_f32_e32 v160, v142, v159
	v_mul_f32_e32 v161, v150, v159
	v_fract_f32_e32 v160, v160
	v_fract_f32_e32 v161, v161
	v_fmac_f32_e32 v160, v159, v146
	v_fmac_f32_e32 v161, v159, v154
	v_cos_f32_e32 v180, v160
	v_sin_f32_e32 v182, v160
	v_cos_f32_e32 v184, v161
	v_sin_f32_e32 v186, v161
	v_mul_f32_e32 v160, v143, v159
	v_mul_f32_e32 v161, v151, v159
	v_fract_f32_e32 v160, v160
	v_fract_f32_e32 v161, v161
	v_fmac_f32_e32 v160, v159, v147
	v_fmac_f32_e32 v161, v159, v155
	v_cos_f32_e32 v181, v160
	v_sin_f32_e32 v183, v160
	v_cos_f32_e32 v185, v161
	v_sin_f32_e32 v187, v161
	v_pk_mul_f32 v[162:163], v[128:129], v[174:175]
	v_pk_mul_f32 v[160:161], v[130:131], v[182:183]
	v_pk_fma_f32 v[162:163], v[136:137], v[172:173], v[162:163] neg_lo:[0,0,1] neg_hi:[0,0,1]
	v_pk_mul_f32 v[166:167], v[124:125], v[178:179]
	v_pk_mul_f32 v[164:165], v[126:127], v[186:187]
	v_pk_mul_f32 v[172:173], v[128:129], v[172:173]
	v_pk_mul_f32 v[128:129], v[130:131], v[180:181]
	v_pk_mul_f32 v[124:125], v[124:125], v[176:177]
	v_pk_mul_f32 v[126:127], v[126:127], v[184:185]
	v_ashrrev_i32_e32 v159, 31, v158
	v_pk_fma_f32 v[160:161], v[138:139], v[180:181], v[160:161] neg_lo:[0,0,1] neg_hi:[0,0,1]
	v_pk_fma_f32 v[164:165], v[134:135], v[184:185], v[164:165] neg_lo:[0,0,1] neg_hi:[0,0,1]
	v_pk_fma_f32 v[166:167], v[132:133], v[176:177], v[166:167] neg_lo:[0,0,1] neg_hi:[0,0,1]
	v_pk_fma_f32 v[128:129], v[138:139], v[182:183], v[128:129]
	v_pk_fma_f32 v[130:131], v[136:137], v[174:175], v[172:173]
	v_pk_fma_f32 v[134:135], v[134:135], v[186:187], v[126:127]
	v_pk_fma_f32 v[132:133], v[132:133], v[178:179], v[124:125]
	v_lshlrev_b64 v[136:137], 11, v[158:159]
	v_lshlrev_b32_e32 v124, 1, v218
	s_cbranch_vccz .LBB0_346
	v_add_u32_e32 v188, s7, v243
	s_movk_i32 s8, 0x1ff
	v_pk_mul_f32 v[138:139], v[160:161], s[76:77] op_sel_hi:[1,0]
	v_pk_mul_f32 v[172:173], v[162:163], s[76:77] op_sel_hi:[1,0]
	v_pk_mul_f32 v[176:177], v[164:165], s[76:77] op_sel_hi:[1,0]
	v_pk_mul_f32 v[174:175], v[166:167], s[76:77] op_sel_hi:[1,0]
	v_pk_mul_f32 v[180:181], v[134:135], s[76:77] op_sel_hi:[1,0]
	v_pk_mul_f32 v[178:179], v[132:133], s[76:77] op_sel_hi:[1,0]
	v_bitop3_b32 v125, v188, s8, v188 bitop3:0xc
	v_cvt_pk_bf16_f32 v172, v172, v173
	v_cvt_pk_bf16_f32 v173, v138, v139
	v_cvt_pk_bf16_f32 v174, v174, v175
	v_cvt_pk_bf16_f32 v175, v176, v177
	v_pk_mul_f32 v[138:139], v[128:129], s[76:77] op_sel_hi:[1,0]
	v_pk_mul_f32 v[176:177], v[130:131], s[76:77] op_sel_hi:[1,0]
	v_cvt_pk_bf16_f32 v178, v178, v179
	v_cvt_pk_bf16_f32 v179, v180, v181
	v_cvt_f32_u32_e32 v125, v125
	v_and_b32_e32 v180, 0x1ff, v188
	v_cvt_pk_bf16_f32 v176, v176, v177
	v_cvt_pk_bf16_f32 v177, v138, v139
	v_cvt_f32_u32_e32 v138, v180
	v_lshl_add_u64 v[126:127], v[156:157], 0, v[136:137]
	global_store_dwordx4 v[126:127], v[172:175], off
	global_store_dwordx4 v[126:127], v[176:179], off offset:256
	v_mul_f32_e32 v125, v171, v125
	v_sub_u32_e32 v127, 0x1fe, v180
	v_exp_f32_e32 v126, v125
	v_mul_f32_e32 v125, v170, v138
	v_cvt_f32_i32_e32 v127, v127
	v_add_u32_e32 v138, 1, v180
	v_cvt_f32_u32_e32 v139, v138
	v_exp_f32_e32 v138, v125
	v_mul_f32_e32 v125, v171, v127
	v_exp_f32_e32 v127, v125
	v_mul_f32_e32 v125, v170, v139
	v_sub_u32_e32 v139, 0x1fd, v180
	v_cvt_f32_i32_e32 v181, v139
	v_add_u32_e32 v139, 2, v180
	v_cvt_f32_u32_e32 v182, v139
	v_exp_f32_e32 v139, v125
	v_mul_f32_e32 v125, v171, v181
	v_sub_u32_e32 v181, 0x1fc, v180
	v_cvt_f32_i32_e32 v181, v181
	v_add_u32_e32 v180, 3, v180
	v_cvt_f32_u32_e32 v180, v180
	v_exp_f32_e32 v184, v125
	v_mul_f32_e32 v125, v170, v182
	v_exp_f32_e32 v186, v125
	v_mul_f32_e32 v125, v171, v181
	v_exp_f32_e32 v185, v125
	v_mul_f32_e32 v125, v170, v180
	v_exp_f32_e32 v187, v125
	v_ashrrev_i32_e32 v125, 10, v188
	v_and_b32_e32 v125, -4, v125
	v_add_u32_e32 v180, s44, v125
	v_ashrrev_i32_e32 v181, 31, v180
	v_lshlrev_b64 v[180:181], 22, v[180:181]
	v_lshlrev_b32_e32 v125, 10, v188
	v_lshl_add_u64 v[180:181], s[40:41], 0, v[180:181]
	v_and_b32_e32 v182, 0x380000, v125
	v_mov_b32_e32 v183, v67
	v_lshlrev_b32_e32 v125, 5, v188
	v_lshl_add_u64 v[180:181], v[180:181], 0, v[182:183]
	v_and_b32_e32 v182, 0x3f00, v125
	v_lshl_add_u64 v[180:181], v[180:181], 0, v[182:183]
	v_mov_b32_e32 v125, v67
	v_lshl_add_u64 v[180:181], v[180:181], 0, v[124:125]
	v_and_b32_e32 v125, 7, v188
	v_lshlrev_b32_e32 v182, 1, v125
	v_lshl_add_u64 v[188:189], v[180:181], 0, v[182:183]
	v_mfma_f32_16x16x32_bf16 v[180:183], v[172:175], v[2:5], 0
	s_lshl_b32 s72, s4, 1
	v_lshl_add_u64 v[188:189], v[188:189], 0, s[72:73]
	s_mov_b32 s8, 0x40000
	v_mfma_f32_16x16x32_bf16 v[172:175], v[172:175], v[6:9], 0
	s_nop 3
	v_mul_f32_e64 v190, v184, v182
	v_mul_f32_e64 v191, v185, v183
	v_pk_mul_f32 v[192:193], v[126:127], v[180:181]
	v_pk_mul_f32 v[182:183], v[186:187], v[182:183]
	v_pk_mul_f32 v[180:181], v[138:139], v[180:181]
	v_cvt_pk_bf16_f32 v192, v192, v193
	v_cvt_pk_bf16_f32 v193, v190, v191
	v_mov_b32_e32 v196, v192
	v_mov_b32_e32 v197, v193
	v_lshl_add_u64 v[200:201], v[188:189], 0, v[202:203]
	v_cvt_pk_bf16_f32 v180, v180, v181
	v_cvt_pk_bf16_f32 v181, v182, v183
	v_add_co_u32_e32 v182, vcc, s8, v188
	s_movk_i32 s8, 0x4000
	s_nop 0
	v_addc_co_u32_e32 v183, vcc, 0, v189, vcc
	v_mov_b32_e32 v198, v180
	v_mov_b32_e32 v199, v181
	s_nop 1
	v_permlane16_swap_b32_e32 v196, v198
	v_permlane16_swap_b32_e32 v197, v199
	global_store_dwordx4 v[200:201], v[196:199], off
	v_pk_mul_f32 v[180:181], v[184:185], v[174:175]
	v_pk_mul_f32 v[182:183], v[126:127], v[172:173]
	v_pk_mul_f32 v[174:175], v[186:187], v[174:175]
	v_cvt_pk_bf16_f32 v182, v182, v183
	v_cvt_pk_bf16_f32 v183, v180, v181
	v_add_co_u32_e32 v180, vcc, s8, v188
	v_pk_mul_f32 v[172:173], v[138:139], v[172:173]
	s_nop 0
	v_addc_co_u32_e32 v181, vcc, 0, v189, vcc
	s_mov_b32 s8, 0x44000
	v_cvt_pk_bf16_f32 v172, v172, v173
	v_cvt_pk_bf16_f32 v173, v174, v175
	v_add_co_u32_e32 v174, vcc, s8, v188
	v_mov_b32_e32 v228, v182
	v_mov_b32_e32 v229, v183
	v_lshl_add_u64 v[232:233], v[180:181], 0, v[202:203]
	s_nop 0
	v_addc_co_u32_e32 v175, vcc, 0, v189, vcc
	v_mov_b32_e32 v230, v172
	v_mov_b32_e32 v231, v173
	s_nop 1
	v_permlane16_swap_b32_e32 v228, v230
	v_permlane16_swap_b32_e32 v229, v231
	global_store_dwordx4 v[232:233], v[228:231], off
	v_mfma_f32_16x16x32_bf16 v[172:175], v[176:179], v[2:5], 0
	s_mov_b32 s8, 0x20000
	s_nop 6
	v_pk_mul_f32 v[180:181], v[184:185], v[174:175]
	v_pk_mul_f32 v[182:183], v[126:127], v[172:173]
	v_pk_mul_f32 v[174:175], v[186:187], v[174:175]
	v_cvt_pk_bf16_f32 v182, v182, v183
	v_cvt_pk_bf16_f32 v183, v180, v181
	v_add_co_u32_e32 v180, vcc, s8, v188
	v_pk_mul_f32 v[172:173], v[138:139], v[172:173]
	s_nop 0
	v_addc_co_u32_e32 v181, vcc, 0, v189, vcc
	s_mov_b32 s8, 0x60000
	v_cvt_pk_bf16_f32 v172, v172, v173
	v_cvt_pk_bf16_f32 v173, v174, v175
	v_add_co_u32_e32 v174, vcc, s8, v188
	s_mov_b32 s8, 0x24000
	s_nop 0
	v_addc_co_u32_e32 v175, vcc, 0, v189, vcc
	v_mov_b32_e32 v198, v172
	v_mov_b32_e32 v199, v173
	v_mfma_f32_16x16x32_bf16 v[172:175], v[176:179], v[6:9], 0
	v_mov_b32_e32 v196, v182
	v_mov_b32_e32 v197, v183
	v_lshl_add_u64 v[200:201], v[180:181], 0, v[202:203]
	s_nop 1
	v_permlane16_swap_b32_e32 v196, v198
	v_permlane16_swap_b32_e32 v197, v199
	global_store_dwordx4 v[200:201], v[196:199], off
	s_nop 6
	v_pk_mul_f32 v[176:177], v[184:185], v[174:175]
	v_pk_mul_f32 v[126:127], v[126:127], v[172:173]
	v_pk_mul_f32 v[138:139], v[138:139], v[172:173]
	v_cvt_pk_bf16_f32 v126, v126, v127
	v_cvt_pk_bf16_f32 v127, v176, v177
	v_add_co_u32_e32 v176, vcc, s8, v188
	v_cvt_pk_bf16_f32 v138, v138, v139
	s_nop 1
	v_addc_co_u32_e32 v177, vcc, 0, v189, vcc
	v_mov_b32_e32 v228, v126
	v_mov_b32_e32 v229, v127
	v_lshl_add_u64 v[232:233], v[176:177], 0, v[202:203]
	v_pk_mul_f32 v[126:127], v[186:187], v[174:175]
	s_nop 0
	v_cvt_pk_bf16_f32 v139, v126, v127
	v_add_co_u32_e32 v126, vcc, 0x64000, v188
	s_nop 1
	v_addc_co_u32_e32 v127, vcc, 0, v189, vcc
	v_mov_b32_e32 v230, v138
	v_mov_b32_e32 v231, v139
	s_nop 1
	v_permlane16_swap_b32_e32 v228, v230
	v_permlane16_swap_b32_e32 v229, v231
	global_store_dwordx4 v[232:233], v[228:231], off
	s_mov_b64 s[8:9], 0xaa00000
	v_lshl_add_u64 v[126:127], v[168:169], 0, s[8:9]
	s_cbranch_execnz .LBB0_322

.LBB0_322:
	s_add_i32 s8, s7, 16
	s_nop 0
	v_add_u32_e32 v128, s8, v205
	v_and_b32_e32 v125, 0xfff, v128
	v_cvt_f32_u32_e32 v125, v125
	s_andn2_b64 vcc, exec, s[34:35]
	v_mul_f32_e32 v129, v140, v125
	v_mul_f32_e32 v130, v148, v125
	v_fract_f32_e32 v129, v129
	v_fract_f32_e32 v130, v130
	v_fmac_f32_e32 v129, v125, v144
	v_fmac_f32_e32 v130, v125, v152
	v_cos_f32_e32 v138, v129
	v_sin_f32_e32 v158, v129
	v_mul_f32_e32 v129, v141, v125
	v_cos_f32_e32 v160, v130
	v_sin_f32_e32 v162, v130
	v_fract_f32_e32 v129, v129
	v_mul_f32_e32 v130, v149, v125
	v_fmac_f32_e32 v129, v125, v145
	v_fract_f32_e32 v130, v130
	v_fmac_f32_e32 v130, v125, v153
	v_cos_f32_e32 v139, v129
	v_sin_f32_e32 v159, v129
	v_mul_f32_e32 v129, v142, v125
	v_cos_f32_e32 v161, v130
	v_sin_f32_e32 v163, v130
	v_fract_f32_e32 v129, v129
	v_mul_f32_e32 v130, v150, v125
	v_fmac_f32_e32 v129, v125, v146
	v_fract_f32_e32 v130, v130
	v_fmac_f32_e32 v130, v125, v154
	v_cos_f32_e32 v164, v129
	v_sin_f32_e32 v166, v129
	v_mul_f32_e32 v129, v143, v125
	v_cos_f32_e32 v168, v130
	v_sin_f32_e32 v172, v130
	v_fract_f32_e32 v129, v129
	v_mul_f32_e32 v130, v151, v125
	v_fmac_f32_e32 v129, v125, v147
	v_fract_f32_e32 v130, v130
	v_fmac_f32_e32 v130, v125, v155
	v_cos_f32_e32 v165, v129
	v_sin_f32_e32 v167, v129
	v_cos_f32_e32 v169, v130
	v_sin_f32_e32 v173, v130
	v_pk_mul_f32 v[132:133], v[112:113], v[158:159]
	v_pk_mul_f32 v[130:131], v[114:115], v[166:167]
	v_pk_fma_f32 v[132:133], v[120:121], v[138:139], v[132:133] neg_lo:[0,0,1] neg_hi:[0,0,1]
	v_pk_mul_f32 v[138:139], v[112:113], v[138:139]
	v_pk_mul_f32 v[136:137], v[108:109], v[162:163]
	v_pk_mul_f32 v[112:113], v[114:115], v[164:165]
	v_pk_fma_f32 v[114:115], v[120:121], v[158:159], v[138:139]
	v_pk_mul_f32 v[120:121], v[108:109], v[160:161]
	v_pk_mul_f32 v[134:135], v[110:111], v[172:173]
	v_pk_fma_f32 v[136:137], v[116:117], v[160:161], v[136:137] neg_lo:[0,0,1] neg_hi:[0,0,1]
	v_pk_mul_f32 v[108:109], v[110:111], v[168:169]
	v_pk_fma_f32 v[110:111], v[116:117], v[162:163], v[120:121]
	v_ashrrev_i32_e32 v129, 31, v128
	v_cndmask_b32_e64 v116, 0, 1, s[34:35]
	v_pk_fma_f32 v[130:131], v[122:123], v[164:165], v[130:131] neg_lo:[0,0,1] neg_hi:[0,0,1]
	v_pk_fma_f32 v[134:135], v[118:119], v[168:169], v[134:135] neg_lo:[0,0,1] neg_hi:[0,0,1]
	v_pk_fma_f32 v[112:113], v[122:123], v[166:167], v[112:113]
	v_pk_fma_f32 v[108:109], v[118:119], v[172:173], v[108:109]
	v_cmp_ne_u32_e64 s[38:39], 1, v116
	v_lshlrev_b64 v[116:117], 11, v[128:129]
	s_cbranch_vccnz .LBB0_347
	v_pk_mul_f32 v[120:121], v[130:131], s[76:77] op_sel_hi:[1,0]
	v_pk_mul_f32 v[118:119], v[132:133], s[76:77] op_sel_hi:[1,0]
	v_pk_mul_f32 v[138:139], v[134:135], s[76:77] op_sel_hi:[1,0]
	v_pk_mul_f32 v[158:159], v[136:137], s[76:77] op_sel_hi:[1,0]
	v_pk_mul_f32 v[162:163], v[108:109], s[76:77] op_sel_hi:[1,0]
	v_pk_mul_f32 v[160:161], v[110:111], s[76:77] op_sel_hi:[1,0]
	v_add_u32_e32 v172, s8, v243
	s_movk_i32 s8, 0x1ff
	v_cvt_pk_bf16_f32 v118, v118, v119
	v_cvt_pk_bf16_f32 v119, v120, v121
	v_cvt_pk_bf16_f32 v120, v158, v159
	v_cvt_pk_bf16_f32 v121, v138, v139
	v_pk_mul_f32 v[138:139], v[112:113], s[76:77] op_sel_hi:[1,0]
	v_pk_mul_f32 v[158:159], v[114:115], s[76:77] op_sel_hi:[1,0]
	v_cvt_pk_bf16_f32 v160, v160, v161
	v_cvt_pk_bf16_f32 v161, v162, v163
	v_bitop3_b32 v125, v172, s8, v172 bitop3:0xc
	v_and_b32_e32 v162, 0x1ff, v172
	v_cvt_pk_bf16_f32 v158, v158, v159
	v_cvt_pk_bf16_f32 v159, v138, v139
	v_cvt_f32_u32_e32 v125, v125
	v_cvt_f32_u32_e32 v138, v162
	v_lshl_add_u64 v[122:123], v[156:157], 0, v[116:117]
	global_store_dwordx4 v[122:123], v[118:121], off
	global_store_dwordx4 v[122:123], v[158:161], off offset:256
	v_mul_f32_e32 v122, v171, v125
	v_mul_f32_e32 v123, v170, v138
	v_sub_u32_e32 v125, 0x1fe, v162
	v_add_u32_e32 v138, 1, v162
	v_cvt_f32_i32_e32 v125, v125
	v_cvt_f32_u32_e32 v139, v138
	v_exp_f32_e32 v138, v123
	v_mov_b32_e32 v165, v67
	v_mul_f32_e32 v123, v171, v125
	v_mul_f32_e32 v125, v170, v139
	v_sub_u32_e32 v139, 0x1fd, v162
	v_cvt_f32_i32_e32 v163, v139
	v_add_u32_e32 v139, 2, v162
	v_cvt_f32_u32_e32 v164, v139
	v_exp_f32_e32 v139, v125
	v_mul_f32_e32 v125, v171, v163
	v_sub_u32_e32 v163, 0x1fc, v162
	v_cvt_f32_i32_e32 v163, v163
	v_add_u32_e32 v162, 3, v162
	v_cvt_f32_u32_e32 v162, v162
	v_exp_f32_e32 v166, v125
	v_mul_f32_e32 v125, v170, v164
	v_exp_f32_e32 v168, v125
	v_mul_f32_e32 v125, v171, v163
	v_exp_f32_e32 v167, v125
	v_mul_f32_e32 v125, v170, v162
	v_exp_f32_e32 v169, v125
	v_ashrrev_i32_e32 v125, 10, v172
	v_and_b32_e32 v125, -4, v125
	v_add_u32_e32 v162, s44, v125
	v_ashrrev_i32_e32 v163, 31, v162
	v_lshlrev_b64 v[162:163], 22, v[162:163]
	v_lshlrev_b32_e32 v125, 10, v172
	v_lshl_add_u64 v[162:163], s[40:41], 0, v[162:163]
	v_and_b32_e32 v164, 0x380000, v125
	v_lshlrev_b32_e32 v125, 5, v172
	v_lshl_add_u64 v[162:163], v[162:163], 0, v[164:165]
	v_and_b32_e32 v164, 0x3f00, v125
	v_lshl_add_u64 v[162:163], v[162:163], 0, v[164:165]
	v_mov_b32_e32 v125, v67
	v_lshl_add_u64 v[162:163], v[162:163], 0, v[124:125]
	v_and_b32_e32 v125, 7, v172
	v_lshlrev_b32_e32 v164, 1, v125
	v_exp_f32_e32 v122, v122
	v_exp_f32_e32 v123, v123
	v_lshl_add_u64 v[172:173], v[162:163], 0, v[164:165]
	v_mfma_f32_16x16x32_bf16 v[162:165], v[118:121], v[2:5], 0
	s_lshl_b32 s72, s4, 1
	v_lshl_add_u64 v[172:173], v[172:173], 0, s[72:73]
	s_mov_b32 s8, 0x40000
	v_mfma_f32_16x16x32_bf16 v[118:121], v[118:121], v[6:9], 0
	s_nop 3
	v_mul_f32_e64 v174, v166, v164
	v_mul_f32_e64 v175, v167, v165
	v_pk_mul_f32 v[176:177], v[122:123], v[162:163]
	v_pk_mul_f32 v[164:165], v[168:169], v[164:165]
	v_pk_mul_f32 v[162:163], v[138:139], v[162:163]
	v_cvt_pk_bf16_f32 v176, v176, v177
	v_cvt_pk_bf16_f32 v177, v174, v175
	v_mov_b32_e32 v196, v176
	v_mov_b32_e32 v197, v177
	v_lshl_add_u64 v[200:201], v[172:173], 0, v[202:203]
	v_cvt_pk_bf16_f32 v162, v162, v163
	v_cvt_pk_bf16_f32 v163, v164, v165
	v_add_co_u32_e32 v164, vcc, s8, v172
	s_movk_i32 s8, 0x4000
	s_nop 0
	v_addc_co_u32_e32 v165, vcc, 0, v173, vcc
	v_mov_b32_e32 v198, v162
	v_mov_b32_e32 v199, v163
	s_nop 1
	v_permlane16_swap_b32_e32 v196, v198
	v_permlane16_swap_b32_e32 v197, v199
	global_store_dwordx4 v[200:201], v[196:199], off
	v_pk_mul_f32 v[162:163], v[166:167], v[120:121]
	v_pk_mul_f32 v[164:165], v[122:123], v[118:119]
	v_pk_mul_f32 v[120:121], v[168:169], v[120:121]
	v_cvt_pk_bf16_f32 v164, v164, v165
	v_cvt_pk_bf16_f32 v165, v162, v163
	v_add_co_u32_e32 v162, vcc, s8, v172
	v_pk_mul_f32 v[118:119], v[138:139], v[118:119]
	s_nop 0
	v_addc_co_u32_e32 v163, vcc, 0, v173, vcc
	s_mov_b32 s8, 0x44000
	v_cvt_pk_bf16_f32 v118, v118, v119
	v_cvt_pk_bf16_f32 v119, v120, v121
	v_add_co_u32_e32 v120, vcc, s8, v172
	v_mov_b32_e32 v228, v164
	v_mov_b32_e32 v229, v165
	v_lshl_add_u64 v[232:233], v[162:163], 0, v[202:203]
	s_nop 0
	v_addc_co_u32_e32 v121, vcc, 0, v173, vcc
	v_mov_b32_e32 v230, v118
	v_mov_b32_e32 v231, v119
	s_nop 1
	v_permlane16_swap_b32_e32 v228, v230
	v_permlane16_swap_b32_e32 v229, v231
	global_store_dwordx4 v[232:233], v[228:231], off
	v_mfma_f32_16x16x32_bf16 v[118:121], v[158:161], v[2:5], 0
	s_mov_b32 s8, 0x20000
	s_nop 6
	v_pk_mul_f32 v[162:163], v[166:167], v[120:121]
	v_pk_mul_f32 v[164:165], v[122:123], v[118:119]
	v_pk_mul_f32 v[120:121], v[168:169], v[120:121]
	v_cvt_pk_bf16_f32 v164, v164, v165
	v_cvt_pk_bf16_f32 v165, v162, v163
	v_add_co_u32_e32 v162, vcc, s8, v172
	v_pk_mul_f32 v[118:119], v[138:139], v[118:119]
	s_nop 0
	v_addc_co_u32_e32 v163, vcc, 0, v173, vcc
	s_mov_b32 s8, 0x60000
	v_cvt_pk_bf16_f32 v118, v118, v119
	v_cvt_pk_bf16_f32 v119, v120, v121
	v_add_co_u32_e32 v120, vcc, s8, v172
	s_mov_b32 s8, 0x24000
	s_nop 0
	v_addc_co_u32_e32 v121, vcc, 0, v173, vcc
	v_mov_b32_e32 v198, v118
	v_mov_b32_e32 v199, v119
	v_mfma_f32_16x16x32_bf16 v[118:121], v[158:161], v[6:9], 0
	v_mov_b32_e32 v196, v164
	v_mov_b32_e32 v197, v165
	v_lshl_add_u64 v[200:201], v[162:163], 0, v[202:203]
	s_nop 1
	v_permlane16_swap_b32_e32 v196, v198
	v_permlane16_swap_b32_e32 v197, v199
	global_store_dwordx4 v[200:201], v[196:199], off
	s_nop 6
	v_pk_mul_f32 v[158:159], v[166:167], v[120:121]
	v_pk_mul_f32 v[122:123], v[122:123], v[118:119]
	v_pk_mul_f32 v[120:121], v[168:169], v[120:121]
	v_cvt_pk_bf16_f32 v122, v122, v123
	v_cvt_pk_bf16_f32 v123, v158, v159
	v_add_co_u32_e32 v158, vcc, s8, v172
	v_pk_mul_f32 v[118:119], v[138:139], v[118:119]
	s_nop 0
	v_addc_co_u32_e32 v159, vcc, 0, v173, vcc
	v_cvt_pk_bf16_f32 v118, v118, v119
	v_cvt_pk_bf16_f32 v119, v120, v121
	v_add_co_u32_e32 v120, vcc, 0x64000, v172
	v_mov_b32_e32 v228, v122
	v_mov_b32_e32 v229, v123
	v_lshl_add_u64 v[232:233], v[158:159], 0, v[202:203]
	s_nop 0
	v_addc_co_u32_e32 v121, vcc, 0, v173, vcc
	v_mov_b32_e32 v230, v118
	v_mov_b32_e32 v231, v119
	s_nop 1
	v_permlane16_swap_b32_e32 v228, v230
	v_permlane16_swap_b32_e32 v229, v231
	global_store_dwordx4 v[232:233], v[228:231], off
	s_cbranch_execnz .LBB0_325

.LBB0_325:
	s_add_i32 s8, s7, 32
	s_nop 0
	v_add_u32_e32 v108, s8, v205
	v_and_b32_e32 v109, 0xfff, v108
	v_cvt_f32_u32_e32 v109, v109
	s_and_b64 vcc, exec, s[38:39]
	v_mul_f32_e32 v110, v140, v109
	v_mul_f32_e32 v111, v148, v109
	v_fract_f32_e32 v110, v110
	v_fract_f32_e32 v111, v111
	v_fmac_f32_e32 v110, v109, v144
	v_fmac_f32_e32 v111, v109, v152
	v_cos_f32_e32 v118, v110
	v_sin_f32_e32 v120, v110
	v_cos_f32_e32 v122, v111
	v_sin_f32_e32 v128, v111
	v_mul_f32_e32 v110, v141, v109
	v_mul_f32_e32 v111, v149, v109
	v_fract_f32_e32 v110, v110
	v_fract_f32_e32 v111, v111
	v_fmac_f32_e32 v110, v109, v145
	v_fmac_f32_e32 v111, v109, v153
	v_cos_f32_e32 v119, v110
	v_sin_f32_e32 v121, v110
	v_cos_f32_e32 v123, v111
	v_sin_f32_e32 v129, v111
	v_mul_f32_e32 v110, v142, v109
	v_mul_f32_e32 v111, v150, v109
	v_fract_f32_e32 v110, v110
	v_fract_f32_e32 v111, v111
	v_fmac_f32_e32 v110, v109, v146
	v_fmac_f32_e32 v111, v109, v154
	v_cos_f32_e32 v130, v110
	v_sin_f32_e32 v132, v110
	v_cos_f32_e32 v134, v111
	v_sin_f32_e32 v136, v111
	v_mul_f32_e32 v110, v143, v109
	v_mul_f32_e32 v111, v151, v109
	v_fract_f32_e32 v110, v110
	v_fract_f32_e32 v111, v111
	v_fmac_f32_e32 v110, v109, v147
	v_fmac_f32_e32 v111, v109, v155
	v_cos_f32_e32 v131, v110
	v_sin_f32_e32 v133, v110
	v_cos_f32_e32 v135, v111
	v_sin_f32_e32 v137, v111
	v_pk_mul_f32 v[112:113], v[96:97], v[120:121]
	v_pk_mul_f32 v[110:111], v[98:99], v[132:133]
	v_pk_fma_f32 v[112:113], v[104:105], v[118:119], v[112:113] neg_lo:[0,0,1] neg_hi:[0,0,1]
	v_pk_mul_f32 v[118:119], v[96:97], v[118:119]
	v_pk_mul_f32 v[116:117], v[92:93], v[128:129]
	v_pk_mul_f32 v[114:115], v[94:95], v[136:137]
	v_pk_mul_f32 v[96:97], v[98:99], v[130:131]
	v_pk_fma_f32 v[98:99], v[104:105], v[120:121], v[118:119]
	v_pk_mul_f32 v[104:105], v[92:93], v[122:123]
	v_pk_mul_f32 v[92:93], v[94:95], v[134:135]
	v_ashrrev_i32_e32 v109, 31, v108
	v_pk_fma_f32 v[110:111], v[106:107], v[130:131], v[110:111] neg_lo:[0,0,1] neg_hi:[0,0,1]
	v_pk_fma_f32 v[114:115], v[102:103], v[134:135], v[114:115] neg_lo:[0,0,1] neg_hi:[0,0,1]
	v_pk_fma_f32 v[116:117], v[100:101], v[122:123], v[116:117] neg_lo:[0,0,1] neg_hi:[0,0,1]
	v_pk_fma_f32 v[96:97], v[106:107], v[132:133], v[96:97]
	v_pk_fma_f32 v[92:93], v[102:103], v[136:137], v[92:93]
	v_pk_fma_f32 v[94:95], v[100:101], v[128:129], v[104:105]
	v_lshlrev_b64 v[100:101], 11, v[108:109]
	s_cbranch_vccnz .LBB0_348
	v_pk_mul_f32 v[104:105], v[110:111], s[76:77] op_sel_hi:[1,0]
	v_pk_mul_f32 v[102:103], v[112:113], s[76:77] op_sel_hi:[1,0]
	v_pk_mul_f32 v[118:119], v[114:115], s[76:77] op_sel_hi:[1,0]
	v_pk_mul_f32 v[120:121], v[116:117], s[76:77] op_sel_hi:[1,0]
	v_cvt_pk_bf16_f32 v102, v102, v103
	v_cvt_pk_bf16_f32 v103, v104, v105
	v_cvt_pk_bf16_f32 v105, v118, v119
	v_pk_mul_f32 v[118:119], v[98:99], s[76:77] op_sel_hi:[1,0]
	v_cvt_pk_bf16_f32 v104, v120, v121
	v_pk_mul_f32 v[120:121], v[96:97], s[76:77] op_sel_hi:[1,0]
	v_pk_mul_f32 v[122:123], v[92:93], s[76:77] op_sel_hi:[1,0]
	v_add_u32_e32 v136, s8, v243
	s_movk_i32 s8, 0x1ff
	v_cvt_pk_bf16_f32 v118, v118, v119
	v_cvt_pk_bf16_f32 v119, v120, v121
	v_cvt_pk_bf16_f32 v121, v122, v123
	v_bitop3_b32 v122, v136, s8, v136 bitop3:0xc
	v_cvt_f32_u32_e32 v122, v122
	v_and_b32_e32 v125, 0x1ff, v136
	v_cvt_f32_u32_e32 v123, v125
	v_lshl_add_u64 v[106:107], v[156:157], 0, v[100:101]
	v_pk_mul_f32 v[128:129], v[94:95], s[76:77] op_sel_hi:[1,0]
	global_store_dwordx4 v[106:107], v[102:105], off
	v_cvt_pk_bf16_f32 v120, v128, v129
	global_store_dwordx4 v[106:107], v[118:121], off offset:256
	v_mul_f32_e32 v106, v171, v122
	v_sub_u32_e32 v122, 0x1fe, v125
	v_mul_f32_e32 v107, v170, v123
	v_cvt_f32_i32_e32 v123, v122
	v_add_u32_e32 v122, 1, v125
	v_cvt_f32_u32_e32 v128, v122
	v_exp_f32_e32 v122, v107
	v_mul_f32_e32 v107, v171, v123
	v_add_u32_e32 v129, 2, v125
	v_mul_f32_e32 v123, v170, v128
	v_sub_u32_e32 v128, 0x1fd, v125
	v_cvt_f32_i32_e32 v128, v128
	v_cvt_f32_u32_e32 v129, v129
	v_mov_b32_e32 v131, v67
	v_exp_f32_e32 v106, v106
	v_mul_f32_e32 v128, v171, v128
	v_exp_f32_e32 v132, v128
	v_mul_f32_e32 v128, v170, v129
	v_sub_u32_e32 v129, 0x1fc, v125
	v_add_u32_e32 v125, 3, v125
	v_cvt_f32_u32_e32 v125, v125
	v_cvt_f32_i32_e32 v129, v129
	v_exp_f32_e32 v134, v128
	v_exp_f32_e32 v107, v107
	v_mul_f32_e32 v125, v170, v125
	v_exp_f32_e32 v135, v125
	v_ashrrev_i32_e32 v125, 10, v136
	v_mul_f32_e32 v128, v171, v129
	v_and_b32_e32 v125, -4, v125
	v_exp_f32_e32 v133, v128
	v_add_u32_e32 v128, s44, v125
	v_ashrrev_i32_e32 v129, 31, v128
	v_lshlrev_b64 v[128:129], 22, v[128:129]
	v_lshlrev_b32_e32 v125, 10, v136
	v_lshl_add_u64 v[128:129], s[40:41], 0, v[128:129]
	v_and_b32_e32 v130, 0x380000, v125
	v_lshlrev_b32_e32 v125, 5, v136
	v_lshl_add_u64 v[128:129], v[128:129], 0, v[130:131]
	v_and_b32_e32 v130, 0x3f00, v125
	v_lshl_add_u64 v[128:129], v[128:129], 0, v[130:131]
	v_mov_b32_e32 v125, v67
	v_lshl_add_u64 v[128:129], v[128:129], 0, v[124:125]
	v_and_b32_e32 v125, 7, v136
	v_lshlrev_b32_e32 v130, 1, v125
	v_exp_f32_e32 v123, v123
	v_lshl_add_u64 v[136:137], v[128:129], 0, v[130:131]
	v_mfma_f32_16x16x32_bf16 v[128:131], v[102:105], v[2:5], 0
	s_lshl_b32 s72, s4, 1
	v_lshl_add_u64 v[136:137], v[136:137], 0, s[72:73]
	s_mov_b32 s8, 0x40000
	v_mfma_f32_16x16x32_bf16 v[102:105], v[102:105], v[6:9], 0
	s_nop 3
	v_mul_f32_e64 v138, v132, v130
	v_mul_f32_e64 v139, v133, v131
	v_pk_mul_f32 v[158:159], v[106:107], v[128:129]
	v_pk_mul_f32 v[130:131], v[134:135], v[130:131]
	v_pk_mul_f32 v[128:129], v[122:123], v[128:129]
	v_cvt_pk_bf16_f32 v158, v158, v159
	v_cvt_pk_bf16_f32 v159, v138, v139
	v_mov_b32_e32 v196, v158
	v_mov_b32_e32 v197, v159
	v_lshl_add_u64 v[200:201], v[136:137], 0, v[202:203]
	v_cvt_pk_bf16_f32 v128, v128, v129
	v_cvt_pk_bf16_f32 v129, v130, v131
	v_add_co_u32_e32 v130, vcc, s8, v136
	s_movk_i32 s8, 0x4000
	s_nop 0
	v_addc_co_u32_e32 v131, vcc, 0, v137, vcc
	v_mov_b32_e32 v198, v128
	v_mov_b32_e32 v199, v129
	s_nop 1
	v_permlane16_swap_b32_e32 v196, v198
	v_permlane16_swap_b32_e32 v197, v199
	global_store_dwordx4 v[200:201], v[196:199], off
	v_pk_mul_f32 v[128:129], v[132:133], v[104:105]
	v_pk_mul_f32 v[130:131], v[106:107], v[102:103]
	v_pk_mul_f32 v[104:105], v[134:135], v[104:105]
	v_cvt_pk_bf16_f32 v130, v130, v131
	v_cvt_pk_bf16_f32 v131, v128, v129
	v_add_co_u32_e32 v128, vcc, s8, v136
	v_pk_mul_f32 v[102:103], v[122:123], v[102:103]
	s_nop 0
	v_addc_co_u32_e32 v129, vcc, 0, v137, vcc
	s_mov_b32 s8, 0x44000
	v_cvt_pk_bf16_f32 v102, v102, v103
	v_cvt_pk_bf16_f32 v103, v104, v105
	v_add_co_u32_e32 v104, vcc, s8, v136
	v_mov_b32_e32 v228, v130
	v_mov_b32_e32 v229, v131
	v_lshl_add_u64 v[232:233], v[128:129], 0, v[202:203]
	s_nop 0
	v_addc_co_u32_e32 v105, vcc, 0, v137, vcc
	v_mov_b32_e32 v230, v102
	v_mov_b32_e32 v231, v103
	s_nop 1
	v_permlane16_swap_b32_e32 v228, v230
	v_permlane16_swap_b32_e32 v229, v231
	global_store_dwordx4 v[232:233], v[228:231], off
	v_mfma_f32_16x16x32_bf16 v[102:105], v[118:121], v[2:5], 0
	s_mov_b32 s8, 0x20000
	s_nop 6
	v_pk_mul_f32 v[128:129], v[132:133], v[104:105]
	v_pk_mul_f32 v[130:131], v[106:107], v[102:103]
	v_pk_mul_f32 v[104:105], v[134:135], v[104:105]
	v_cvt_pk_bf16_f32 v130, v130, v131
	v_cvt_pk_bf16_f32 v131, v128, v129
	v_add_co_u32_e32 v128, vcc, s8, v136
	v_pk_mul_f32 v[102:103], v[122:123], v[102:103]
	s_nop 0
	v_addc_co_u32_e32 v129, vcc, 0, v137, vcc
	s_mov_b32 s8, 0x60000
	v_cvt_pk_bf16_f32 v102, v102, v103
	v_cvt_pk_bf16_f32 v103, v104, v105
	v_add_co_u32_e32 v104, vcc, s8, v136
	s_mov_b32 s8, 0x24000
	s_nop 0
	v_addc_co_u32_e32 v105, vcc, 0, v137, vcc
	v_mov_b32_e32 v198, v102
	v_mov_b32_e32 v199, v103
	v_mfma_f32_16x16x32_bf16 v[102:105], v[118:121], v[6:9], 0
	v_mov_b32_e32 v196, v130
	v_mov_b32_e32 v197, v131
	v_lshl_add_u64 v[200:201], v[128:129], 0, v[202:203]
	s_nop 1
	v_permlane16_swap_b32_e32 v196, v198
	v_permlane16_swap_b32_e32 v197, v199
	global_store_dwordx4 v[200:201], v[196:199], off
	s_nop 6
	v_pk_mul_f32 v[118:119], v[132:133], v[104:105]
	v_pk_mul_f32 v[106:107], v[106:107], v[102:103]
	v_pk_mul_f32 v[104:105], v[134:135], v[104:105]
	v_cvt_pk_bf16_f32 v106, v106, v107
	v_cvt_pk_bf16_f32 v107, v118, v119
	v_add_co_u32_e32 v118, vcc, s8, v136
	v_pk_mul_f32 v[102:103], v[122:123], v[102:103]
	s_nop 0
	v_addc_co_u32_e32 v119, vcc, 0, v137, vcc
	v_cvt_pk_bf16_f32 v102, v102, v103
	v_cvt_pk_bf16_f32 v103, v104, v105
	v_add_co_u32_e32 v104, vcc, 0x64000, v136
	v_mov_b32_e32 v228, v106
	v_mov_b32_e32 v229, v107
	v_lshl_add_u64 v[232:233], v[118:119], 0, v[202:203]
	s_nop 0
	v_addc_co_u32_e32 v105, vcc, 0, v137, vcc
	v_mov_b32_e32 v230, v102
	v_mov_b32_e32 v231, v103
	s_nop 1
	v_permlane16_swap_b32_e32 v228, v230
	v_permlane16_swap_b32_e32 v229, v231
	global_store_dwordx4 v[232:233], v[228:231], off
	s_cbranch_execnz .LBB0_328

.LBB0_328:
	s_add_i32 s8, s7, 48
	s_nop 0
	v_add_u32_e32 v92, s8, v205
	v_and_b32_e32 v93, 0xfff, v92
	v_cvt_f32_u32_e32 v93, v93
	s_and_b64 vcc, exec, s[38:39]
	v_mul_f32_e32 v94, v140, v93
	v_mul_f32_e32 v95, v148, v93
	v_fract_f32_e32 v94, v94
	v_fract_f32_e32 v95, v95
	v_fmac_f32_e32 v94, v93, v144
	v_fmac_f32_e32 v95, v93, v152
	v_cos_f32_e32 v102, v94
	v_sin_f32_e32 v104, v94
	v_cos_f32_e32 v106, v95
	v_sin_f32_e32 v108, v95
	v_mul_f32_e32 v94, v141, v93
	v_mul_f32_e32 v95, v149, v93
	v_fract_f32_e32 v94, v94
	v_fract_f32_e32 v95, v95
	v_fmac_f32_e32 v94, v93, v145
	v_fmac_f32_e32 v95, v93, v153
	v_cos_f32_e32 v103, v94
	v_sin_f32_e32 v105, v94
	v_cos_f32_e32 v107, v95
	v_sin_f32_e32 v109, v95
	v_mul_f32_e32 v94, v142, v93
	v_mul_f32_e32 v95, v150, v93
	v_fract_f32_e32 v94, v94
	v_fract_f32_e32 v95, v95
	v_fmac_f32_e32 v94, v93, v146
	v_fmac_f32_e32 v95, v93, v154
	v_cos_f32_e32 v110, v94
	v_sin_f32_e32 v112, v94
	v_cos_f32_e32 v114, v95
	v_sin_f32_e32 v116, v95
	v_mul_f32_e32 v94, v143, v93
	v_mul_f32_e32 v95, v151, v93
	v_fract_f32_e32 v94, v94
	v_fract_f32_e32 v95, v95
	v_fmac_f32_e32 v94, v93, v147
	v_fmac_f32_e32 v95, v93, v155
	v_cos_f32_e32 v111, v94
	v_sin_f32_e32 v113, v94
	v_cos_f32_e32 v115, v95
	v_sin_f32_e32 v117, v95
	v_pk_mul_f32 v[96:97], v[80:81], v[104:105]
	v_pk_mul_f32 v[94:95], v[82:83], v[112:113]
	v_pk_fma_f32 v[96:97], v[88:89], v[102:103], v[96:97] neg_lo:[0,0,1] neg_hi:[0,0,1]
	v_pk_mul_f32 v[102:103], v[80:81], v[102:103]
	v_pk_mul_f32 v[100:101], v[76:77], v[108:109]
	v_pk_mul_f32 v[98:99], v[78:79], v[116:117]
	v_pk_mul_f32 v[80:81], v[82:83], v[110:111]
	v_pk_fma_f32 v[82:83], v[88:89], v[104:105], v[102:103]
	v_pk_mul_f32 v[88:89], v[76:77], v[106:107]
	v_pk_mul_f32 v[76:77], v[78:79], v[114:115]
	v_ashrrev_i32_e32 v93, 31, v92
	v_pk_fma_f32 v[94:95], v[90:91], v[110:111], v[94:95] neg_lo:[0,0,1] neg_hi:[0,0,1]
	v_pk_fma_f32 v[98:99], v[86:87], v[114:115], v[98:99] neg_lo:[0,0,1] neg_hi:[0,0,1]
	v_pk_fma_f32 v[100:101], v[84:85], v[106:107], v[100:101] neg_lo:[0,0,1] neg_hi:[0,0,1]
	v_pk_fma_f32 v[80:81], v[90:91], v[112:113], v[80:81]
	v_pk_fma_f32 v[76:77], v[86:87], v[116:117], v[76:77]
	v_pk_fma_f32 v[78:79], v[84:85], v[108:109], v[88:89]
	v_lshlrev_b64 v[84:85], 11, v[92:93]
	s_cbranch_vccnz .LBB0_349
	v_pk_mul_f32 v[88:89], v[94:95], s[76:77] op_sel_hi:[1,0]
	v_pk_mul_f32 v[86:87], v[96:97], s[76:77] op_sel_hi:[1,0]
	v_pk_mul_f32 v[102:103], v[98:99], s[76:77] op_sel_hi:[1,0]
	v_pk_mul_f32 v[104:105], v[100:101], s[76:77] op_sel_hi:[1,0]
	v_cvt_pk_bf16_f32 v86, v86, v87
	v_cvt_pk_bf16_f32 v87, v88, v89
	v_cvt_pk_bf16_f32 v89, v102, v103
	v_pk_mul_f32 v[102:103], v[82:83], s[76:77] op_sel_hi:[1,0]
	v_cvt_pk_bf16_f32 v88, v104, v105
	v_pk_mul_f32 v[104:105], v[80:81], s[76:77] op_sel_hi:[1,0]
	v_pk_mul_f32 v[106:107], v[76:77], s[76:77] op_sel_hi:[1,0]
	v_add_u32_e32 v116, s8, v243
	s_movk_i32 s8, 0x1ff
	v_pk_mul_f32 v[108:109], v[78:79], s[76:77] op_sel_hi:[1,0]
	v_cvt_pk_bf16_f32 v102, v102, v103
	v_cvt_pk_bf16_f32 v103, v104, v105
	v_cvt_pk_bf16_f32 v105, v106, v107
	v_bitop3_b32 v106, v116, s8, v116 bitop3:0xc
	v_and_b32_e32 v107, 0x1ff, v116
	v_cvt_pk_bf16_f32 v104, v108, v109
	v_cvt_f32_u32_e32 v106, v106
	v_cvt_f32_u32_e32 v108, v107
	v_lshl_add_u64 v[90:91], v[156:157], 0, v[84:85]
	global_store_dwordx4 v[90:91], v[86:89], off
	global_store_dwordx4 v[90:91], v[102:105], off offset:256
	v_mul_f32_e32 v90, v171, v106
	v_mul_f32_e32 v91, v170, v108
	v_sub_u32_e32 v106, 0x1fe, v107
	v_add_u32_e32 v108, 1, v107
	v_cvt_f32_i32_e32 v106, v106
	v_cvt_f32_u32_e32 v108, v108
	v_exp_f32_e32 v110, v91
	v_add_u32_e32 v109, 2, v107
	v_mul_f32_e32 v91, v171, v106
	v_mul_f32_e32 v106, v170, v108
	v_sub_u32_e32 v108, 0x1fd, v107
	v_cvt_f32_i32_e32 v108, v108
	v_cvt_f32_u32_e32 v109, v109
	v_exp_f32_e32 v111, v106
	v_mov_b32_e32 v125, v67
	v_mul_f32_e32 v106, v171, v108
	v_sub_u32_e32 v108, 0x1fc, v107
	v_cvt_f32_i32_e32 v108, v108
	v_add_u32_e32 v107, 3, v107
	v_cvt_f32_u32_e32 v107, v107
	v_exp_f32_e32 v112, v106
	v_mul_f32_e32 v106, v170, v109
	v_exp_f32_e32 v114, v106
	v_mul_f32_e32 v106, v171, v108
	v_exp_f32_e32 v113, v106
	v_mul_f32_e32 v106, v170, v107
	v_exp_f32_e32 v115, v106
	v_ashrrev_i32_e32 v106, 10, v116
	v_and_b32_e32 v106, -4, v106
	v_add_u32_e32 v106, s44, v106
	v_ashrrev_i32_e32 v107, 31, v106
	v_lshlrev_b64 v[106:107], 22, v[106:107]
	v_lshlrev_b32_e32 v108, 10, v116
	v_lshl_add_u64 v[106:107], s[40:41], 0, v[106:107]
	v_and_b32_e32 v108, 0x380000, v108
	v_mov_b32_e32 v109, v67
	v_lshl_add_u64 v[106:107], v[106:107], 0, v[108:109]
	v_lshlrev_b32_e32 v108, 5, v116
	v_and_b32_e32 v108, 0x3f00, v108
	v_lshl_add_u64 v[106:107], v[106:107], 0, v[108:109]
	v_and_b32_e32 v108, 7, v116
	v_lshl_add_u64 v[106:107], v[106:107], 0, v[124:125]
	v_lshlrev_b32_e32 v108, 1, v108
	v_exp_f32_e32 v90, v90
	v_exp_f32_e32 v91, v91
	v_lshl_add_u64 v[116:117], v[106:107], 0, v[108:109]
	v_mfma_f32_16x16x32_bf16 v[106:109], v[86:89], v[2:5], 0
	s_lshl_b32 s72, s4, 1
	v_lshl_add_u64 v[116:117], v[116:117], 0, s[72:73]
	s_mov_b32 s8, 0x40000
	v_mfma_f32_16x16x32_bf16 v[86:89], v[86:89], v[6:9], 0
	s_nop 3
	v_mul_f32_e64 v118, v112, v108
	v_mul_f32_e64 v119, v113, v109
	v_pk_mul_f32 v[120:121], v[90:91], v[106:107]
	v_pk_mul_f32 v[108:109], v[114:115], v[108:109]
	v_pk_mul_f32 v[106:107], v[110:111], v[106:107]
	v_cvt_pk_bf16_f32 v120, v120, v121
	v_cvt_pk_bf16_f32 v121, v118, v119
	v_mov_b32_e32 v196, v120
	v_mov_b32_e32 v197, v121
	v_lshl_add_u64 v[200:201], v[116:117], 0, v[202:203]
	v_cvt_pk_bf16_f32 v106, v106, v107
	v_cvt_pk_bf16_f32 v107, v108, v109
	v_add_co_u32_e32 v108, vcc, s8, v116
	s_movk_i32 s8, 0x4000
	s_nop 0
	v_addc_co_u32_e32 v109, vcc, 0, v117, vcc
	v_mov_b32_e32 v198, v106
	v_mov_b32_e32 v199, v107
	s_nop 1
	v_permlane16_swap_b32_e32 v196, v198
	v_permlane16_swap_b32_e32 v197, v199
	global_store_dwordx4 v[200:201], v[196:199], off
	v_pk_mul_f32 v[106:107], v[112:113], v[88:89]
	v_pk_mul_f32 v[108:109], v[90:91], v[86:87]
	v_pk_mul_f32 v[88:89], v[114:115], v[88:89]
	v_cvt_pk_bf16_f32 v108, v108, v109
	v_cvt_pk_bf16_f32 v109, v106, v107
	v_add_co_u32_e32 v106, vcc, s8, v116
	v_pk_mul_f32 v[86:87], v[110:111], v[86:87]
	s_nop 0
	v_addc_co_u32_e32 v107, vcc, 0, v117, vcc
	s_mov_b32 s8, 0x44000
	v_cvt_pk_bf16_f32 v86, v86, v87
	v_cvt_pk_bf16_f32 v87, v88, v89
	v_add_co_u32_e32 v88, vcc, s8, v116
	v_mov_b32_e32 v228, v108
	v_mov_b32_e32 v229, v109
	v_lshl_add_u64 v[232:233], v[106:107], 0, v[202:203]
	s_nop 0
	v_addc_co_u32_e32 v89, vcc, 0, v117, vcc
	v_mov_b32_e32 v230, v86
	v_mov_b32_e32 v231, v87
	s_nop 1
	v_permlane16_swap_b32_e32 v228, v230
	v_permlane16_swap_b32_e32 v229, v231
	global_store_dwordx4 v[232:233], v[228:231], off
	v_mfma_f32_16x16x32_bf16 v[86:89], v[102:105], v[2:5], 0
	s_mov_b32 s8, 0x20000
	s_nop 6
	v_pk_mul_f32 v[106:107], v[112:113], v[88:89]
	v_pk_mul_f32 v[108:109], v[90:91], v[86:87]
	v_pk_mul_f32 v[88:89], v[114:115], v[88:89]
	v_cvt_pk_bf16_f32 v108, v108, v109
	v_cvt_pk_bf16_f32 v109, v106, v107
	v_add_co_u32_e32 v106, vcc, s8, v116
	v_pk_mul_f32 v[86:87], v[110:111], v[86:87]
	s_nop 0
	v_addc_co_u32_e32 v107, vcc, 0, v117, vcc
	s_mov_b32 s8, 0x60000
	v_cvt_pk_bf16_f32 v86, v86, v87
	v_cvt_pk_bf16_f32 v87, v88, v89
	v_add_co_u32_e32 v88, vcc, s8, v116
	s_mov_b32 s8, 0x24000
	s_nop 0
	v_addc_co_u32_e32 v89, vcc, 0, v117, vcc
	v_mov_b32_e32 v198, v86
	v_mov_b32_e32 v199, v87
	v_mfma_f32_16x16x32_bf16 v[86:89], v[102:105], v[6:9], 0
	v_mov_b32_e32 v196, v108
	v_mov_b32_e32 v197, v109
	v_lshl_add_u64 v[200:201], v[106:107], 0, v[202:203]
	s_nop 1
	v_permlane16_swap_b32_e32 v196, v198
	v_permlane16_swap_b32_e32 v197, v199
	global_store_dwordx4 v[200:201], v[196:199], off
	s_nop 6
	v_pk_mul_f32 v[102:103], v[112:113], v[88:89]
	v_pk_mul_f32 v[90:91], v[90:91], v[86:87]
	v_pk_mul_f32 v[88:89], v[114:115], v[88:89]
	v_cvt_pk_bf16_f32 v90, v90, v91
	v_cvt_pk_bf16_f32 v91, v102, v103
	v_add_co_u32_e32 v102, vcc, s8, v116
	v_pk_mul_f32 v[86:87], v[110:111], v[86:87]
	s_nop 0
	v_addc_co_u32_e32 v103, vcc, 0, v117, vcc
	v_cvt_pk_bf16_f32 v86, v86, v87
	v_cvt_pk_bf16_f32 v87, v88, v89
	v_add_co_u32_e32 v88, vcc, 0x64000, v116
	v_mov_b32_e32 v228, v90
	v_mov_b32_e32 v229, v91
	v_lshl_add_u64 v[232:233], v[102:103], 0, v[202:203]
	s_nop 0
	v_addc_co_u32_e32 v89, vcc, 0, v117, vcc
	v_mov_b32_e32 v230, v86
	v_mov_b32_e32 v231, v87
	s_nop 1
	v_permlane16_swap_b32_e32 v228, v230
	v_permlane16_swap_b32_e32 v229, v231
	global_store_dwordx4 v[232:233], v[228:231], off
	s_cbranch_execnz .LBB0_331

.LBB0_331:
	s_add_i32 s8, s7, 0x80
	s_nop 0
	v_add_u32_e32 v76, s8, v205
	v_and_b32_e32 v77, 0xfff, v76
	v_cvt_f32_u32_e32 v77, v77
	s_and_b64 vcc, exec, s[38:39]
	v_mul_f32_e32 v78, v140, v77
	v_mul_f32_e32 v79, v148, v77
	v_fract_f32_e32 v78, v78
	v_fract_f32_e32 v79, v79
	v_fmac_f32_e32 v78, v77, v144
	v_fmac_f32_e32 v79, v77, v152
	v_cos_f32_e32 v86, v78
	v_sin_f32_e32 v88, v78
	v_cos_f32_e32 v90, v79
	v_sin_f32_e32 v92, v79
	v_mul_f32_e32 v78, v141, v77
	v_mul_f32_e32 v79, v149, v77
	v_fract_f32_e32 v78, v78
	v_fract_f32_e32 v79, v79
	v_fmac_f32_e32 v78, v77, v145
	v_fmac_f32_e32 v79, v77, v153
	v_cos_f32_e32 v87, v78
	v_sin_f32_e32 v89, v78
	v_cos_f32_e32 v91, v79
	v_sin_f32_e32 v93, v79
	v_mul_f32_e32 v78, v142, v77
	v_mul_f32_e32 v79, v150, v77
	v_fract_f32_e32 v78, v78
	v_fract_f32_e32 v79, v79
	v_fmac_f32_e32 v78, v77, v146
	v_fmac_f32_e32 v79, v77, v154
	v_cos_f32_e32 v94, v78
	v_sin_f32_e32 v96, v78
	v_cos_f32_e32 v98, v79
	v_sin_f32_e32 v100, v79
	v_mul_f32_e32 v78, v143, v77
	v_mul_f32_e32 v79, v151, v77
	v_fract_f32_e32 v78, v78
	v_fract_f32_e32 v79, v79
	v_fmac_f32_e32 v78, v77, v147
	v_fmac_f32_e32 v79, v77, v155
	v_cos_f32_e32 v95, v78
	v_sin_f32_e32 v97, v78
	v_cos_f32_e32 v99, v79
	v_sin_f32_e32 v101, v79
	v_pk_mul_f32 v[80:81], v[62:63], v[88:89]
	v_pk_mul_f32 v[78:79], v[64:65], v[96:97]
	v_pk_fma_f32 v[80:81], v[72:73], v[86:87], v[80:81] neg_lo:[0,0,1] neg_hi:[0,0,1]
	v_pk_mul_f32 v[86:87], v[62:63], v[86:87]
	v_pk_mul_f32 v[84:85], v[58:59], v[92:93]
	v_pk_mul_f32 v[82:83], v[60:61], v[100:101]
	v_pk_mul_f32 v[62:63], v[64:65], v[94:95]
	v_pk_fma_f32 v[64:65], v[72:73], v[88:89], v[86:87]
	v_pk_mul_f32 v[72:73], v[58:59], v[90:91]
	v_pk_mul_f32 v[58:59], v[60:61], v[98:99]
	v_ashrrev_i32_e32 v77, 31, v76
	v_pk_fma_f32 v[78:79], v[74:75], v[94:95], v[78:79] neg_lo:[0,0,1] neg_hi:[0,0,1]
	v_pk_fma_f32 v[82:83], v[70:71], v[98:99], v[82:83] neg_lo:[0,0,1] neg_hi:[0,0,1]
	v_pk_fma_f32 v[84:85], v[68:69], v[90:91], v[84:85] neg_lo:[0,0,1] neg_hi:[0,0,1]
	v_pk_fma_f32 v[62:63], v[74:75], v[96:97], v[62:63]
	v_pk_fma_f32 v[58:59], v[70:71], v[100:101], v[58:59]
	v_pk_fma_f32 v[60:61], v[68:69], v[92:93], v[72:73]
	v_lshlrev_b64 v[68:69], 11, v[76:77]
	s_cbranch_vccnz .LBB0_350
	v_pk_mul_f32 v[72:73], v[78:79], s[76:77] op_sel_hi:[1,0]
	v_pk_mul_f32 v[70:71], v[80:81], s[76:77] op_sel_hi:[1,0]
	v_pk_mul_f32 v[86:87], v[82:83], s[76:77] op_sel_hi:[1,0]
	v_pk_mul_f32 v[88:89], v[84:85], s[76:77] op_sel_hi:[1,0]
	v_cvt_pk_bf16_f32 v70, v70, v71
	v_cvt_pk_bf16_f32 v71, v72, v73
	v_cvt_pk_bf16_f32 v73, v86, v87
	v_pk_mul_f32 v[86:87], v[64:65], s[76:77] op_sel_hi:[1,0]
	v_cvt_pk_bf16_f32 v72, v88, v89
	v_pk_mul_f32 v[88:89], v[62:63], s[76:77] op_sel_hi:[1,0]
	v_pk_mul_f32 v[90:91], v[58:59], s[76:77] op_sel_hi:[1,0]
	v_add_u32_e32 v100, s8, v243
	s_movk_i32 s8, 0x1ff
	v_pk_mul_f32 v[92:93], v[60:61], s[76:77] op_sel_hi:[1,0]
	v_cvt_pk_bf16_f32 v86, v86, v87
	v_cvt_pk_bf16_f32 v87, v88, v89
	v_cvt_pk_bf16_f32 v89, v90, v91
	v_bitop3_b32 v90, v100, s8, v100 bitop3:0xc
	v_and_b32_e32 v91, 0x1ff, v100
	v_cvt_pk_bf16_f32 v88, v92, v93
	v_cvt_f32_u32_e32 v90, v90
	v_cvt_f32_u32_e32 v92, v91
	v_lshl_add_u64 v[74:75], v[156:157], 0, v[68:69]
	global_store_dwordx4 v[74:75], v[70:73], off
	global_store_dwordx4 v[74:75], v[86:89], off offset:256
	v_mul_f32_e32 v74, v171, v90
	v_mul_f32_e32 v75, v170, v92
	v_sub_u32_e32 v90, 0x1fe, v91
	v_add_u32_e32 v92, 1, v91
	v_cvt_f32_i32_e32 v90, v90
	v_cvt_f32_u32_e32 v92, v92
	v_exp_f32_e32 v94, v75
	v_add_u32_e32 v93, 2, v91
	v_mul_f32_e32 v75, v171, v90
	v_mul_f32_e32 v90, v170, v92
	v_sub_u32_e32 v92, 0x1fd, v91
	v_cvt_f32_i32_e32 v92, v92
	v_cvt_f32_u32_e32 v93, v93
	v_exp_f32_e32 v95, v90
	v_mov_b32_e32 v125, v67
	v_mul_f32_e32 v90, v171, v92
	v_sub_u32_e32 v92, 0x1fc, v91
	v_cvt_f32_i32_e32 v92, v92
	v_add_u32_e32 v91, 3, v91
	v_cvt_f32_u32_e32 v91, v91
	v_exp_f32_e32 v96, v90
	v_mul_f32_e32 v90, v170, v93
	v_exp_f32_e32 v98, v90
	v_mul_f32_e32 v90, v171, v92
	v_exp_f32_e32 v97, v90
	v_mul_f32_e32 v90, v170, v91
	v_exp_f32_e32 v99, v90
	v_ashrrev_i32_e32 v90, 10, v100
	v_and_b32_e32 v90, -4, v90
	v_add_u32_e32 v90, s44, v90
	v_ashrrev_i32_e32 v91, 31, v90
	v_lshlrev_b64 v[90:91], 22, v[90:91]
	v_lshlrev_b32_e32 v92, 10, v100
	v_lshl_add_u64 v[90:91], s[40:41], 0, v[90:91]
	v_and_b32_e32 v92, 0x380000, v92
	v_mov_b32_e32 v93, v67
	v_lshl_add_u64 v[90:91], v[90:91], 0, v[92:93]
	v_lshlrev_b32_e32 v92, 5, v100
	v_and_b32_e32 v92, 0x3f00, v92
	v_lshl_add_u64 v[90:91], v[90:91], 0, v[92:93]
	v_and_b32_e32 v92, 7, v100
	v_lshl_add_u64 v[90:91], v[90:91], 0, v[124:125]
	v_lshlrev_b32_e32 v92, 1, v92
	v_exp_f32_e32 v74, v74
	v_exp_f32_e32 v75, v75
	v_lshl_add_u64 v[100:101], v[90:91], 0, v[92:93]
	v_mfma_f32_16x16x32_bf16 v[90:93], v[70:73], v[2:5], 0
	s_lshl_b32 s72, s4, 1
	v_lshl_add_u64 v[100:101], v[100:101], 0, s[72:73]
	s_mov_b32 s8, 0x40000
	v_mfma_f32_16x16x32_bf16 v[70:73], v[70:73], v[6:9], 0
	s_nop 3
	v_mul_f32_e64 v102, v96, v92
	v_mul_f32_e64 v103, v97, v93
	v_pk_mul_f32 v[104:105], v[74:75], v[90:91]
	v_pk_mul_f32 v[92:93], v[98:99], v[92:93]
	v_pk_mul_f32 v[90:91], v[94:95], v[90:91]
	v_cvt_pk_bf16_f32 v104, v104, v105
	v_cvt_pk_bf16_f32 v105, v102, v103
	v_mov_b32_e32 v196, v104
	v_mov_b32_e32 v197, v105
	v_lshl_add_u64 v[200:201], v[100:101], 0, v[202:203]
	v_cvt_pk_bf16_f32 v90, v90, v91
	v_cvt_pk_bf16_f32 v91, v92, v93
	v_add_co_u32_e32 v92, vcc, s8, v100
	s_movk_i32 s8, 0x4000
	s_nop 0
	v_addc_co_u32_e32 v93, vcc, 0, v101, vcc
	v_mov_b32_e32 v198, v90
	v_mov_b32_e32 v199, v91
	s_nop 1
	v_permlane16_swap_b32_e32 v196, v198
	v_permlane16_swap_b32_e32 v197, v199
	global_store_dwordx4 v[200:201], v[196:199], off
	v_pk_mul_f32 v[90:91], v[96:97], v[72:73]
	v_pk_mul_f32 v[92:93], v[74:75], v[70:71]
	v_pk_mul_f32 v[72:73], v[98:99], v[72:73]
	v_cvt_pk_bf16_f32 v92, v92, v93
	v_cvt_pk_bf16_f32 v93, v90, v91
	v_add_co_u32_e32 v90, vcc, s8, v100
	v_pk_mul_f32 v[70:71], v[94:95], v[70:71]
	s_nop 0
	v_addc_co_u32_e32 v91, vcc, 0, v101, vcc
	s_mov_b32 s8, 0x44000
	v_cvt_pk_bf16_f32 v70, v70, v71
	v_cvt_pk_bf16_f32 v71, v72, v73
	v_add_co_u32_e32 v72, vcc, s8, v100
	v_mov_b32_e32 v228, v92
	v_mov_b32_e32 v229, v93
	v_lshl_add_u64 v[232:233], v[90:91], 0, v[202:203]
	s_nop 0
	v_addc_co_u32_e32 v73, vcc, 0, v101, vcc
	v_mov_b32_e32 v230, v70
	v_mov_b32_e32 v231, v71
	s_nop 1
	v_permlane16_swap_b32_e32 v228, v230
	v_permlane16_swap_b32_e32 v229, v231
	global_store_dwordx4 v[232:233], v[228:231], off
	v_mfma_f32_16x16x32_bf16 v[70:73], v[86:89], v[2:5], 0
	s_mov_b32 s8, 0x20000
	s_nop 6
	v_pk_mul_f32 v[90:91], v[96:97], v[72:73]
	v_pk_mul_f32 v[92:93], v[74:75], v[70:71]
	v_pk_mul_f32 v[72:73], v[98:99], v[72:73]
	v_cvt_pk_bf16_f32 v92, v92, v93
	v_cvt_pk_bf16_f32 v93, v90, v91
	v_add_co_u32_e32 v90, vcc, s8, v100
	v_pk_mul_f32 v[70:71], v[94:95], v[70:71]
	s_nop 0
	v_addc_co_u32_e32 v91, vcc, 0, v101, vcc
	s_mov_b32 s8, 0x60000
	v_cvt_pk_bf16_f32 v70, v70, v71
	v_cvt_pk_bf16_f32 v71, v72, v73
	v_add_co_u32_e32 v72, vcc, s8, v100
	s_mov_b32 s8, 0x24000
	s_nop 0
	v_addc_co_u32_e32 v73, vcc, 0, v101, vcc
	v_mov_b32_e32 v198, v70
	v_mov_b32_e32 v199, v71
	v_mfma_f32_16x16x32_bf16 v[70:73], v[86:89], v[6:9], 0
	v_mov_b32_e32 v196, v92
	v_mov_b32_e32 v197, v93
	v_lshl_add_u64 v[200:201], v[90:91], 0, v[202:203]
	s_nop 1
	v_permlane16_swap_b32_e32 v196, v198
	v_permlane16_swap_b32_e32 v197, v199
	global_store_dwordx4 v[200:201], v[196:199], off
	s_nop 6
	v_pk_mul_f32 v[86:87], v[96:97], v[72:73]
	v_pk_mul_f32 v[74:75], v[74:75], v[70:71]
	v_pk_mul_f32 v[72:73], v[98:99], v[72:73]
	v_cvt_pk_bf16_f32 v74, v74, v75
	v_cvt_pk_bf16_f32 v75, v86, v87
	v_add_co_u32_e32 v86, vcc, s8, v100
	v_pk_mul_f32 v[70:71], v[94:95], v[70:71]
	s_nop 0
	v_addc_co_u32_e32 v87, vcc, 0, v101, vcc
	v_cvt_pk_bf16_f32 v70, v70, v71
	v_cvt_pk_bf16_f32 v71, v72, v73
	v_add_co_u32_e32 v72, vcc, 0x64000, v100
	v_mov_b32_e32 v228, v74
	v_mov_b32_e32 v229, v75
	v_lshl_add_u64 v[232:233], v[86:87], 0, v[202:203]
	s_nop 0
	v_addc_co_u32_e32 v73, vcc, 0, v101, vcc
	v_mov_b32_e32 v230, v70
	v_mov_b32_e32 v231, v71
	s_nop 1
	v_permlane16_swap_b32_e32 v228, v230
	v_permlane16_swap_b32_e32 v229, v231
	global_store_dwordx4 v[232:233], v[228:231], off
	s_cbranch_execnz .LBB0_334

.LBB0_334:
	s_add_i32 s8, s7, 0x90
	s_nop 0
	v_add_u32_e32 v58, s8, v205
	v_and_b32_e32 v59, 0xfff, v58
	v_cvt_f32_u32_e32 v59, v59
	s_and_b64 vcc, exec, s[38:39]
	v_mul_f32_e32 v60, v140, v59
	v_mul_f32_e32 v61, v148, v59
	v_fract_f32_e32 v60, v60
	v_fract_f32_e32 v61, v61
	v_fmac_f32_e32 v60, v59, v144
	v_fmac_f32_e32 v61, v59, v152
	v_cos_f32_e32 v70, v60
	v_sin_f32_e32 v72, v60
	v_cos_f32_e32 v74, v61
	v_sin_f32_e32 v76, v61
	v_mul_f32_e32 v60, v141, v59
	v_mul_f32_e32 v61, v149, v59
	v_fract_f32_e32 v60, v60
	v_fract_f32_e32 v61, v61
	v_fmac_f32_e32 v60, v59, v145
	v_fmac_f32_e32 v61, v59, v153
	v_cos_f32_e32 v71, v60
	v_sin_f32_e32 v73, v60
	v_cos_f32_e32 v75, v61
	v_sin_f32_e32 v77, v61
	v_mul_f32_e32 v60, v142, v59
	v_mul_f32_e32 v61, v150, v59
	v_fract_f32_e32 v60, v60
	v_fract_f32_e32 v61, v61
	v_fmac_f32_e32 v60, v59, v146
	v_fmac_f32_e32 v61, v59, v154
	v_cos_f32_e32 v78, v60
	v_sin_f32_e32 v80, v60
	v_cos_f32_e32 v82, v61
	v_sin_f32_e32 v84, v61
	v_mul_f32_e32 v60, v143, v59
	v_mul_f32_e32 v61, v151, v59
	v_fract_f32_e32 v60, v60
	v_fract_f32_e32 v61, v61
	v_fmac_f32_e32 v60, v59, v147
	v_fmac_f32_e32 v61, v59, v155
	v_cos_f32_e32 v79, v60
	v_sin_f32_e32 v81, v60
	v_cos_f32_e32 v83, v61
	v_sin_f32_e32 v85, v61
	v_pk_mul_f32 v[62:63], v[46:47], v[72:73]
	v_pk_mul_f32 v[60:61], v[48:49], v[80:81]
	v_pk_fma_f32 v[62:63], v[54:55], v[70:71], v[62:63] neg_lo:[0,0,1] neg_hi:[0,0,1]
	v_pk_mul_f32 v[70:71], v[46:47], v[70:71]
	v_pk_mul_f32 v[68:69], v[42:43], v[76:77]
	v_pk_mul_f32 v[64:65], v[44:45], v[84:85]
	v_pk_mul_f32 v[46:47], v[48:49], v[78:79]
	v_pk_fma_f32 v[48:49], v[54:55], v[72:73], v[70:71]
	v_pk_mul_f32 v[54:55], v[42:43], v[74:75]
	v_pk_mul_f32 v[42:43], v[44:45], v[82:83]
	v_ashrrev_i32_e32 v59, 31, v58
	v_pk_fma_f32 v[60:61], v[56:57], v[78:79], v[60:61] neg_lo:[0,0,1] neg_hi:[0,0,1]
	v_pk_fma_f32 v[64:65], v[52:53], v[82:83], v[64:65] neg_lo:[0,0,1] neg_hi:[0,0,1]
	v_pk_fma_f32 v[68:69], v[50:51], v[74:75], v[68:69] neg_lo:[0,0,1] neg_hi:[0,0,1]
	v_pk_fma_f32 v[46:47], v[56:57], v[80:81], v[46:47]
	v_pk_fma_f32 v[42:43], v[52:53], v[84:85], v[42:43]
	v_pk_fma_f32 v[44:45], v[50:51], v[76:77], v[54:55]
	v_lshlrev_b64 v[50:51], 11, v[58:59]
	s_cbranch_vccnz .LBB0_351
	v_pk_mul_f32 v[54:55], v[60:61], s[76:77] op_sel_hi:[1,0]
	v_pk_mul_f32 v[52:53], v[62:63], s[76:77] op_sel_hi:[1,0]
	v_pk_mul_f32 v[70:71], v[64:65], s[76:77] op_sel_hi:[1,0]
	v_pk_mul_f32 v[72:73], v[68:69], s[76:77] op_sel_hi:[1,0]
	v_cvt_pk_bf16_f32 v52, v52, v53
	v_cvt_pk_bf16_f32 v53, v54, v55
	v_cvt_pk_bf16_f32 v55, v70, v71
	v_pk_mul_f32 v[70:71], v[48:49], s[76:77] op_sel_hi:[1,0]
	v_cvt_pk_bf16_f32 v54, v72, v73
	v_pk_mul_f32 v[72:73], v[46:47], s[76:77] op_sel_hi:[1,0]
	v_pk_mul_f32 v[74:75], v[42:43], s[76:77] op_sel_hi:[1,0]
	v_add_u32_e32 v84, s8, v243
	s_movk_i32 s8, 0x1ff
	v_pk_mul_f32 v[76:77], v[44:45], s[76:77] op_sel_hi:[1,0]
	v_cvt_pk_bf16_f32 v70, v70, v71
	v_cvt_pk_bf16_f32 v71, v72, v73
	v_cvt_pk_bf16_f32 v73, v74, v75
	v_bitop3_b32 v74, v84, s8, v84 bitop3:0xc
	v_and_b32_e32 v75, 0x1ff, v84
	v_cvt_pk_bf16_f32 v72, v76, v77
	v_cvt_f32_u32_e32 v74, v74
	v_cvt_f32_u32_e32 v76, v75
	v_lshl_add_u64 v[56:57], v[156:157], 0, v[50:51]
	global_store_dwordx4 v[56:57], v[52:55], off
	global_store_dwordx4 v[56:57], v[70:73], off offset:256
	v_mul_f32_e32 v56, v171, v74
	v_mul_f32_e32 v57, v170, v76
	v_sub_u32_e32 v74, 0x1fe, v75
	v_add_u32_e32 v76, 1, v75
	v_cvt_f32_i32_e32 v74, v74
	v_cvt_f32_u32_e32 v76, v76
	v_exp_f32_e32 v78, v57
	v_add_u32_e32 v77, 2, v75
	v_mul_f32_e32 v57, v171, v74
	v_mul_f32_e32 v74, v170, v76
	v_sub_u32_e32 v76, 0x1fd, v75
	v_cvt_f32_i32_e32 v76, v76
	v_cvt_f32_u32_e32 v77, v77
	v_exp_f32_e32 v79, v74
	v_mov_b32_e32 v125, v67
	v_mul_f32_e32 v74, v171, v76
	v_sub_u32_e32 v76, 0x1fc, v75
	v_cvt_f32_i32_e32 v76, v76
	v_add_u32_e32 v75, 3, v75
	v_cvt_f32_u32_e32 v75, v75
	v_exp_f32_e32 v80, v74
	v_mul_f32_e32 v74, v170, v77
	v_exp_f32_e32 v82, v74
	v_mul_f32_e32 v74, v171, v76
	v_exp_f32_e32 v81, v74
	v_mul_f32_e32 v74, v170, v75
	v_exp_f32_e32 v83, v74
	v_ashrrev_i32_e32 v74, 10, v84
	v_and_b32_e32 v74, -4, v74
	v_add_u32_e32 v74, s44, v74
	v_ashrrev_i32_e32 v75, 31, v74
	v_lshlrev_b64 v[74:75], 22, v[74:75]
	v_lshlrev_b32_e32 v76, 10, v84
	v_lshl_add_u64 v[74:75], s[40:41], 0, v[74:75]
	v_and_b32_e32 v76, 0x380000, v76
	v_mov_b32_e32 v77, v67
	v_lshl_add_u64 v[74:75], v[74:75], 0, v[76:77]
	v_lshlrev_b32_e32 v76, 5, v84
	v_and_b32_e32 v76, 0x3f00, v76
	v_lshl_add_u64 v[74:75], v[74:75], 0, v[76:77]
	v_and_b32_e32 v76, 7, v84
	v_lshl_add_u64 v[74:75], v[74:75], 0, v[124:125]
	v_lshlrev_b32_e32 v76, 1, v76
	v_exp_f32_e32 v56, v56
	v_exp_f32_e32 v57, v57
	v_lshl_add_u64 v[84:85], v[74:75], 0, v[76:77]
	v_mfma_f32_16x16x32_bf16 v[74:77], v[52:55], v[2:5], 0
	s_lshl_b32 s72, s4, 1
	v_lshl_add_u64 v[84:85], v[84:85], 0, s[72:73]
	s_mov_b32 s8, 0x40000
	v_mfma_f32_16x16x32_bf16 v[52:55], v[52:55], v[6:9], 0
	s_nop 3
	v_mul_f32_e64 v86, v80, v76
	v_mul_f32_e64 v87, v81, v77
	v_pk_mul_f32 v[88:89], v[56:57], v[74:75]
	v_pk_mul_f32 v[76:77], v[82:83], v[76:77]
	v_pk_mul_f32 v[74:75], v[78:79], v[74:75]
	v_cvt_pk_bf16_f32 v88, v88, v89
	v_cvt_pk_bf16_f32 v89, v86, v87
	v_mov_b32_e32 v196, v88
	v_mov_b32_e32 v197, v89
	v_lshl_add_u64 v[200:201], v[84:85], 0, v[202:203]
	v_cvt_pk_bf16_f32 v74, v74, v75
	v_cvt_pk_bf16_f32 v75, v76, v77
	v_add_co_u32_e32 v76, vcc, s8, v84
	s_movk_i32 s8, 0x4000
	s_nop 0
	v_addc_co_u32_e32 v77, vcc, 0, v85, vcc
	v_mov_b32_e32 v198, v74
	v_mov_b32_e32 v199, v75
	s_nop 1
	v_permlane16_swap_b32_e32 v196, v198
	v_permlane16_swap_b32_e32 v197, v199
	global_store_dwordx4 v[200:201], v[196:199], off
	v_pk_mul_f32 v[74:75], v[80:81], v[54:55]
	v_pk_mul_f32 v[76:77], v[56:57], v[52:53]
	v_pk_mul_f32 v[54:55], v[82:83], v[54:55]
	v_cvt_pk_bf16_f32 v76, v76, v77
	v_cvt_pk_bf16_f32 v77, v74, v75
	v_add_co_u32_e32 v74, vcc, s8, v84
	v_pk_mul_f32 v[52:53], v[78:79], v[52:53]
	s_nop 0
	v_addc_co_u32_e32 v75, vcc, 0, v85, vcc
	s_mov_b32 s8, 0x44000
	v_cvt_pk_bf16_f32 v52, v52, v53
	v_cvt_pk_bf16_f32 v53, v54, v55
	v_add_co_u32_e32 v54, vcc, s8, v84
	v_mov_b32_e32 v228, v76
	v_mov_b32_e32 v229, v77
	v_lshl_add_u64 v[232:233], v[74:75], 0, v[202:203]
	s_nop 0
	v_addc_co_u32_e32 v55, vcc, 0, v85, vcc
	v_mov_b32_e32 v230, v52
	v_mov_b32_e32 v231, v53
	s_nop 1
	v_permlane16_swap_b32_e32 v228, v230
	v_permlane16_swap_b32_e32 v229, v231
	global_store_dwordx4 v[232:233], v[228:231], off
	v_mfma_f32_16x16x32_bf16 v[52:55], v[70:73], v[2:5], 0
	s_mov_b32 s8, 0x20000
	s_nop 6
	v_pk_mul_f32 v[74:75], v[80:81], v[54:55]
	v_pk_mul_f32 v[76:77], v[56:57], v[52:53]
	v_pk_mul_f32 v[54:55], v[82:83], v[54:55]
	v_cvt_pk_bf16_f32 v76, v76, v77
	v_cvt_pk_bf16_f32 v77, v74, v75
	v_add_co_u32_e32 v74, vcc, s8, v84
	v_pk_mul_f32 v[52:53], v[78:79], v[52:53]
	s_nop 0
	v_addc_co_u32_e32 v75, vcc, 0, v85, vcc
	s_mov_b32 s8, 0x60000
	v_cvt_pk_bf16_f32 v52, v52, v53
	v_cvt_pk_bf16_f32 v53, v54, v55
	v_add_co_u32_e32 v54, vcc, s8, v84
	s_mov_b32 s8, 0x24000
	s_nop 0
	v_addc_co_u32_e32 v55, vcc, 0, v85, vcc
	v_mov_b32_e32 v198, v52
	v_mov_b32_e32 v199, v53
	v_mfma_f32_16x16x32_bf16 v[52:55], v[70:73], v[6:9], 0
	v_mov_b32_e32 v196, v76
	v_mov_b32_e32 v197, v77
	v_lshl_add_u64 v[200:201], v[74:75], 0, v[202:203]
	s_nop 1
	v_permlane16_swap_b32_e32 v196, v198
	v_permlane16_swap_b32_e32 v197, v199
	global_store_dwordx4 v[200:201], v[196:199], off
	s_nop 6
	v_pk_mul_f32 v[70:71], v[80:81], v[54:55]
	v_pk_mul_f32 v[56:57], v[56:57], v[52:53]
	v_pk_mul_f32 v[54:55], v[82:83], v[54:55]
	v_cvt_pk_bf16_f32 v56, v56, v57
	v_cvt_pk_bf16_f32 v57, v70, v71
	v_add_co_u32_e32 v70, vcc, s8, v84
	v_pk_mul_f32 v[52:53], v[78:79], v[52:53]
	s_nop 0
	v_addc_co_u32_e32 v71, vcc, 0, v85, vcc
	v_cvt_pk_bf16_f32 v52, v52, v53
	v_cvt_pk_bf16_f32 v53, v54, v55
	v_add_co_u32_e32 v54, vcc, 0x64000, v84
	v_mov_b32_e32 v228, v56
	v_mov_b32_e32 v229, v57
	v_lshl_add_u64 v[232:233], v[70:71], 0, v[202:203]
	s_nop 0
	v_addc_co_u32_e32 v55, vcc, 0, v85, vcc
	v_mov_b32_e32 v230, v52
	v_mov_b32_e32 v231, v53
	s_nop 1
	v_permlane16_swap_b32_e32 v228, v230
	v_permlane16_swap_b32_e32 v229, v231
	global_store_dwordx4 v[232:233], v[228:231], off
	s_cbranch_execnz .LBB0_337

.LBB0_337:
	s_add_i32 s8, s7, 0xa0
	s_nop 0
	v_add_u32_e32 v42, s8, v205
	v_and_b32_e32 v43, 0xfff, v42
	v_cvt_f32_u32_e32 v43, v43
	s_and_b64 vcc, exec, s[38:39]
	v_mul_f32_e32 v44, v140, v43
	v_mul_f32_e32 v45, v148, v43
	v_fract_f32_e32 v44, v44
	v_fract_f32_e32 v45, v45
	v_fmac_f32_e32 v44, v43, v144
	v_fmac_f32_e32 v45, v43, v152
	v_cos_f32_e32 v52, v44
	v_sin_f32_e32 v54, v44
	v_cos_f32_e32 v56, v45
	v_sin_f32_e32 v58, v45
	v_mul_f32_e32 v44, v141, v43
	v_mul_f32_e32 v45, v149, v43
	v_fract_f32_e32 v44, v44
	v_fract_f32_e32 v45, v45
	v_fmac_f32_e32 v44, v43, v145
	v_fmac_f32_e32 v45, v43, v153
	v_cos_f32_e32 v53, v44
	v_sin_f32_e32 v55, v44
	v_cos_f32_e32 v57, v45
	v_sin_f32_e32 v59, v45
	v_mul_f32_e32 v44, v142, v43
	v_mul_f32_e32 v45, v150, v43
	v_fract_f32_e32 v44, v44
	v_fract_f32_e32 v45, v45
	v_fmac_f32_e32 v44, v43, v146
	v_fmac_f32_e32 v45, v43, v154
	v_cos_f32_e32 v60, v44
	v_sin_f32_e32 v62, v44
	v_cos_f32_e32 v64, v45
	v_sin_f32_e32 v68, v45
	v_mul_f32_e32 v44, v143, v43
	v_mul_f32_e32 v45, v151, v43
	v_fract_f32_e32 v44, v44
	v_fract_f32_e32 v45, v45
	v_fmac_f32_e32 v44, v43, v147
	v_fmac_f32_e32 v45, v43, v155
	v_cos_f32_e32 v61, v44
	v_sin_f32_e32 v63, v44
	v_cos_f32_e32 v65, v45
	v_sin_f32_e32 v69, v45
	v_pk_mul_f32 v[46:47], v[30:31], v[54:55]
	v_pk_mul_f32 v[44:45], v[32:33], v[62:63]
	v_pk_fma_f32 v[46:47], v[38:39], v[52:53], v[46:47] neg_lo:[0,0,1] neg_hi:[0,0,1]
	v_pk_mul_f32 v[52:53], v[30:31], v[52:53]
	v_pk_mul_f32 v[50:51], v[26:27], v[58:59]
	v_pk_mul_f32 v[48:49], v[28:29], v[68:69]
	v_pk_mul_f32 v[30:31], v[32:33], v[60:61]
	v_pk_fma_f32 v[32:33], v[38:39], v[54:55], v[52:53]
	v_pk_mul_f32 v[38:39], v[26:27], v[56:57]
	v_pk_mul_f32 v[26:27], v[28:29], v[64:65]
	v_ashrrev_i32_e32 v43, 31, v42
	v_pk_fma_f32 v[44:45], v[40:41], v[60:61], v[44:45] neg_lo:[0,0,1] neg_hi:[0,0,1]
	v_pk_fma_f32 v[48:49], v[36:37], v[64:65], v[48:49] neg_lo:[0,0,1] neg_hi:[0,0,1]
	v_pk_fma_f32 v[50:51], v[34:35], v[56:57], v[50:51] neg_lo:[0,0,1] neg_hi:[0,0,1]
	v_pk_fma_f32 v[30:31], v[40:41], v[62:63], v[30:31]
	v_pk_fma_f32 v[26:27], v[36:37], v[68:69], v[26:27]
	v_pk_fma_f32 v[28:29], v[34:35], v[58:59], v[38:39]
	v_lshlrev_b64 v[34:35], 11, v[42:43]
	s_cbranch_vccnz .LBB0_352
	v_pk_mul_f32 v[38:39], v[44:45], s[76:77] op_sel_hi:[1,0]
	v_pk_mul_f32 v[36:37], v[46:47], s[76:77] op_sel_hi:[1,0]
	v_pk_mul_f32 v[52:53], v[48:49], s[76:77] op_sel_hi:[1,0]
	v_pk_mul_f32 v[54:55], v[50:51], s[76:77] op_sel_hi:[1,0]
	v_cvt_pk_bf16_f32 v36, v36, v37
	v_cvt_pk_bf16_f32 v37, v38, v39
	v_cvt_pk_bf16_f32 v39, v52, v53
	v_pk_mul_f32 v[52:53], v[32:33], s[76:77] op_sel_hi:[1,0]
	v_cvt_pk_bf16_f32 v38, v54, v55
	v_pk_mul_f32 v[54:55], v[30:31], s[76:77] op_sel_hi:[1,0]
	v_pk_mul_f32 v[56:57], v[26:27], s[76:77] op_sel_hi:[1,0]
	v_add_u32_e32 v68, s8, v243
	s_movk_i32 s8, 0x1ff
	v_pk_mul_f32 v[58:59], v[28:29], s[76:77] op_sel_hi:[1,0]
	v_cvt_pk_bf16_f32 v52, v52, v53
	v_cvt_pk_bf16_f32 v53, v54, v55
	v_cvt_pk_bf16_f32 v55, v56, v57
	v_bitop3_b32 v56, v68, s8, v68 bitop3:0xc
	v_and_b32_e32 v57, 0x1ff, v68
	v_cvt_pk_bf16_f32 v54, v58, v59
	v_cvt_f32_u32_e32 v56, v56
	v_cvt_f32_u32_e32 v58, v57
	v_lshl_add_u64 v[40:41], v[156:157], 0, v[34:35]
	global_store_dwordx4 v[40:41], v[36:39], off
	global_store_dwordx4 v[40:41], v[52:55], off offset:256
	v_mul_f32_e32 v40, v171, v56
	v_mul_f32_e32 v41, v170, v58
	v_sub_u32_e32 v56, 0x1fe, v57
	v_add_u32_e32 v58, 1, v57
	v_cvt_f32_i32_e32 v56, v56
	v_cvt_f32_u32_e32 v58, v58
	v_exp_f32_e32 v60, v41
	v_add_u32_e32 v59, 2, v57
	v_mul_f32_e32 v41, v171, v56
	v_mul_f32_e32 v56, v170, v58
	v_sub_u32_e32 v58, 0x1fd, v57
	v_cvt_f32_i32_e32 v58, v58
	v_cvt_f32_u32_e32 v59, v59
	v_exp_f32_e32 v61, v56
	v_mov_b32_e32 v125, v67
	v_mul_f32_e32 v56, v171, v58
	v_sub_u32_e32 v58, 0x1fc, v57
	v_cvt_f32_i32_e32 v58, v58
	v_add_u32_e32 v57, 3, v57
	v_cvt_f32_u32_e32 v57, v57
	v_exp_f32_e32 v62, v56
	v_mul_f32_e32 v56, v170, v59
	v_exp_f32_e32 v64, v56
	v_mul_f32_e32 v56, v171, v58
	v_exp_f32_e32 v63, v56
	v_mul_f32_e32 v56, v170, v57
	v_exp_f32_e32 v65, v56
	v_ashrrev_i32_e32 v56, 10, v68
	v_and_b32_e32 v56, -4, v56
	v_add_u32_e32 v56, s44, v56
	v_ashrrev_i32_e32 v57, 31, v56
	v_lshlrev_b64 v[56:57], 22, v[56:57]
	v_lshlrev_b32_e32 v58, 10, v68
	v_lshl_add_u64 v[56:57], s[40:41], 0, v[56:57]
	v_and_b32_e32 v58, 0x380000, v58
	v_mov_b32_e32 v59, v67
	v_lshl_add_u64 v[56:57], v[56:57], 0, v[58:59]
	v_lshlrev_b32_e32 v58, 5, v68
	v_and_b32_e32 v58, 0x3f00, v58
	v_lshl_add_u64 v[56:57], v[56:57], 0, v[58:59]
	v_and_b32_e32 v58, 7, v68
	v_lshl_add_u64 v[56:57], v[56:57], 0, v[124:125]
	v_lshlrev_b32_e32 v58, 1, v58
	v_exp_f32_e32 v40, v40
	v_exp_f32_e32 v41, v41
	v_lshl_add_u64 v[68:69], v[56:57], 0, v[58:59]
	v_mfma_f32_16x16x32_bf16 v[56:59], v[36:39], v[2:5], 0
	s_lshl_b32 s72, s4, 1
	v_lshl_add_u64 v[68:69], v[68:69], 0, s[72:73]
	s_mov_b32 s8, 0x40000
	v_mfma_f32_16x16x32_bf16 v[36:39], v[36:39], v[6:9], 0
	s_nop 3
	v_mul_f32_e64 v70, v62, v58
	v_mul_f32_e64 v71, v63, v59
	v_pk_mul_f32 v[72:73], v[40:41], v[56:57]
	v_pk_mul_f32 v[58:59], v[64:65], v[58:59]
	v_pk_mul_f32 v[56:57], v[60:61], v[56:57]
	v_cvt_pk_bf16_f32 v72, v72, v73
	v_cvt_pk_bf16_f32 v73, v70, v71
	v_mov_b32_e32 v196, v72
	v_mov_b32_e32 v197, v73
	v_lshl_add_u64 v[200:201], v[68:69], 0, v[202:203]
	v_cvt_pk_bf16_f32 v56, v56, v57
	v_cvt_pk_bf16_f32 v57, v58, v59
	v_add_co_u32_e32 v58, vcc, s8, v68
	s_movk_i32 s8, 0x4000
	s_nop 0
	v_addc_co_u32_e32 v59, vcc, 0, v69, vcc
	v_mov_b32_e32 v198, v56
	v_mov_b32_e32 v199, v57
	s_nop 1
	v_permlane16_swap_b32_e32 v196, v198
	v_permlane16_swap_b32_e32 v197, v199
	global_store_dwordx4 v[200:201], v[196:199], off
	v_pk_mul_f32 v[56:57], v[62:63], v[38:39]
	v_pk_mul_f32 v[58:59], v[40:41], v[36:37]
	v_pk_mul_f32 v[38:39], v[64:65], v[38:39]
	v_cvt_pk_bf16_f32 v58, v58, v59
	v_cvt_pk_bf16_f32 v59, v56, v57
	v_add_co_u32_e32 v56, vcc, s8, v68
	v_pk_mul_f32 v[36:37], v[60:61], v[36:37]
	s_nop 0
	v_addc_co_u32_e32 v57, vcc, 0, v69, vcc
	s_mov_b32 s8, 0x44000
	v_cvt_pk_bf16_f32 v36, v36, v37
	v_cvt_pk_bf16_f32 v37, v38, v39
	v_add_co_u32_e32 v38, vcc, s8, v68
	v_mov_b32_e32 v228, v58
	v_mov_b32_e32 v229, v59
	v_lshl_add_u64 v[232:233], v[56:57], 0, v[202:203]
	s_nop 0
	v_addc_co_u32_e32 v39, vcc, 0, v69, vcc
	v_mov_b32_e32 v230, v36
	v_mov_b32_e32 v231, v37
	s_nop 1
	v_permlane16_swap_b32_e32 v228, v230
	v_permlane16_swap_b32_e32 v229, v231
	global_store_dwordx4 v[232:233], v[228:231], off
	v_mfma_f32_16x16x32_bf16 v[36:39], v[52:55], v[2:5], 0
	s_mov_b32 s8, 0x20000
	s_nop 6
	v_pk_mul_f32 v[56:57], v[62:63], v[38:39]
	v_pk_mul_f32 v[58:59], v[40:41], v[36:37]
	v_pk_mul_f32 v[38:39], v[64:65], v[38:39]
	v_cvt_pk_bf16_f32 v58, v58, v59
	v_cvt_pk_bf16_f32 v59, v56, v57
	v_add_co_u32_e32 v56, vcc, s8, v68
	v_pk_mul_f32 v[36:37], v[60:61], v[36:37]
	s_nop 0
	v_addc_co_u32_e32 v57, vcc, 0, v69, vcc
	s_mov_b32 s8, 0x60000
	v_cvt_pk_bf16_f32 v36, v36, v37
	v_cvt_pk_bf16_f32 v37, v38, v39
	v_add_co_u32_e32 v38, vcc, s8, v68
	s_mov_b32 s8, 0x24000
	s_nop 0
	v_addc_co_u32_e32 v39, vcc, 0, v69, vcc
	v_mov_b32_e32 v198, v36
	v_mov_b32_e32 v199, v37
	v_mfma_f32_16x16x32_bf16 v[36:39], v[52:55], v[6:9], 0
	v_mov_b32_e32 v196, v58
	v_mov_b32_e32 v197, v59
	v_lshl_add_u64 v[200:201], v[56:57], 0, v[202:203]
	s_nop 1
	v_permlane16_swap_b32_e32 v196, v198
	v_permlane16_swap_b32_e32 v197, v199
	global_store_dwordx4 v[200:201], v[196:199], off
	s_nop 6
	v_pk_mul_f32 v[52:53], v[62:63], v[38:39]
	v_pk_mul_f32 v[40:41], v[40:41], v[36:37]
	v_pk_mul_f32 v[38:39], v[64:65], v[38:39]
	v_cvt_pk_bf16_f32 v40, v40, v41
	v_cvt_pk_bf16_f32 v41, v52, v53
	v_add_co_u32_e32 v52, vcc, s8, v68
	v_pk_mul_f32 v[36:37], v[60:61], v[36:37]
	s_nop 0
	v_addc_co_u32_e32 v53, vcc, 0, v69, vcc
	v_cvt_pk_bf16_f32 v36, v36, v37
	v_cvt_pk_bf16_f32 v37, v38, v39
	v_add_co_u32_e32 v38, vcc, 0x64000, v68
	v_mov_b32_e32 v228, v40
	v_mov_b32_e32 v229, v41
	v_lshl_add_u64 v[232:233], v[52:53], 0, v[202:203]
	s_nop 0
	v_addc_co_u32_e32 v39, vcc, 0, v69, vcc
	v_mov_b32_e32 v230, v36
	v_mov_b32_e32 v231, v37
	s_nop 1
	v_permlane16_swap_b32_e32 v228, v230
	v_permlane16_swap_b32_e32 v229, v231
	global_store_dwordx4 v[232:233], v[228:231], off
	s_cbranch_execnz .LBB0_340

.LBB0_340:
	s_addk_i32 s7, 0xb0
	s_nop 0
	v_add_u32_e32 v26, s7, v205
	v_and_b32_e32 v27, 0xfff, v26
	v_cvt_f32_u32_e32 v27, v27
	s_and_b64 vcc, exec, s[38:39]
	v_mul_f32_e32 v28, v140, v27
	v_mul_f32_e32 v29, v148, v27
	v_fract_f32_e32 v28, v28
	v_fract_f32_e32 v29, v29
	v_fmac_f32_e32 v28, v27, v144
	v_fmac_f32_e32 v29, v27, v152
	v_cos_f32_e32 v36, v28
	v_sin_f32_e32 v38, v28
	v_cos_f32_e32 v40, v29
	v_sin_f32_e32 v42, v29
	v_mul_f32_e32 v28, v141, v27
	v_mul_f32_e32 v29, v149, v27
	v_fract_f32_e32 v28, v28
	v_fract_f32_e32 v29, v29
	v_fmac_f32_e32 v28, v27, v145
	v_fmac_f32_e32 v29, v27, v153
	v_cos_f32_e32 v37, v28
	v_sin_f32_e32 v39, v28
	v_cos_f32_e32 v41, v29
	v_sin_f32_e32 v43, v29
	v_mul_f32_e32 v28, v142, v27
	v_mul_f32_e32 v29, v150, v27
	v_fract_f32_e32 v28, v28
	v_fract_f32_e32 v29, v29
	v_fmac_f32_e32 v28, v27, v146
	v_fmac_f32_e32 v29, v27, v154
	v_cos_f32_e32 v44, v28
	v_sin_f32_e32 v46, v28
	v_cos_f32_e32 v48, v29
	v_sin_f32_e32 v50, v29
	v_mul_f32_e32 v28, v143, v27
	v_mul_f32_e32 v29, v151, v27
	v_fract_f32_e32 v28, v28
	v_fract_f32_e32 v29, v29
	v_fmac_f32_e32 v28, v27, v147
	v_fmac_f32_e32 v29, v27, v155
	v_cos_f32_e32 v45, v28
	v_sin_f32_e32 v47, v28
	v_cos_f32_e32 v49, v29
	v_sin_f32_e32 v51, v29
	v_pk_mul_f32 v[30:31], v[14:15], v[38:39]
	v_pk_mul_f32 v[28:29], v[16:17], v[46:47]
	v_pk_fma_f32 v[30:31], v[22:23], v[36:37], v[30:31] neg_lo:[0,0,1] neg_hi:[0,0,1]
	v_pk_mul_f32 v[36:37], v[14:15], v[36:37]
	v_pk_mul_f32 v[34:35], v[10:11], v[42:43]
	v_pk_mul_f32 v[32:33], v[12:13], v[50:51]
	v_pk_mul_f32 v[14:15], v[16:17], v[44:45]
	v_pk_fma_f32 v[16:17], v[22:23], v[38:39], v[36:37]
	v_pk_mul_f32 v[22:23], v[10:11], v[40:41]
	v_pk_mul_f32 v[10:11], v[12:13], v[48:49]
	v_ashrrev_i32_e32 v27, 31, v26
	v_pk_fma_f32 v[28:29], v[24:25], v[44:45], v[28:29] neg_lo:[0,0,1] neg_hi:[0,0,1]
	v_pk_fma_f32 v[32:33], v[20:21], v[48:49], v[32:33] neg_lo:[0,0,1] neg_hi:[0,0,1]
	v_pk_fma_f32 v[34:35], v[18:19], v[40:41], v[34:35] neg_lo:[0,0,1] neg_hi:[0,0,1]
	v_pk_fma_f32 v[14:15], v[24:25], v[46:47], v[14:15]
	v_pk_fma_f32 v[10:11], v[20:21], v[50:51], v[10:11]
	v_pk_fma_f32 v[12:13], v[18:19], v[42:43], v[22:23]
	v_lshlrev_b64 v[18:19], 11, v[26:27]
	s_cbranch_vccnz .LBB0_353
	v_pk_mul_f32 v[22:23], v[28:29], s[76:77] op_sel_hi:[1,0]
	v_pk_mul_f32 v[20:21], v[30:31], s[76:77] op_sel_hi:[1,0]
	v_pk_mul_f32 v[36:37], v[32:33], s[76:77] op_sel_hi:[1,0]
	v_pk_mul_f32 v[38:39], v[34:35], s[76:77] op_sel_hi:[1,0]
	v_cvt_pk_bf16_f32 v20, v20, v21
	v_cvt_pk_bf16_f32 v21, v22, v23
	v_cvt_pk_bf16_f32 v23, v36, v37
	v_pk_mul_f32 v[36:37], v[16:17], s[76:77] op_sel_hi:[1,0]
	v_cvt_pk_bf16_f32 v22, v38, v39
	v_pk_mul_f32 v[38:39], v[14:15], s[76:77] op_sel_hi:[1,0]
	v_pk_mul_f32 v[40:41], v[10:11], s[76:77] op_sel_hi:[1,0]
	v_add_u32_e32 v50, s7, v243
	s_movk_i32 s7, 0x1ff
	v_pk_mul_f32 v[42:43], v[12:13], s[76:77] op_sel_hi:[1,0]
	v_cvt_pk_bf16_f32 v36, v36, v37
	v_cvt_pk_bf16_f32 v37, v38, v39
	v_cvt_pk_bf16_f32 v39, v40, v41
	v_bitop3_b32 v40, v50, s7, v50 bitop3:0xc
	v_and_b32_e32 v41, 0x1ff, v50
	v_cvt_pk_bf16_f32 v38, v42, v43
	v_cvt_f32_u32_e32 v40, v40
	v_cvt_f32_u32_e32 v42, v41
	v_lshl_add_u64 v[24:25], v[156:157], 0, v[18:19]
	global_store_dwordx4 v[24:25], v[20:23], off
	global_store_dwordx4 v[24:25], v[36:39], off offset:256
	v_mul_f32_e32 v24, v171, v40
	v_mul_f32_e32 v25, v170, v42
	v_sub_u32_e32 v40, 0x1fe, v41
	v_add_u32_e32 v42, 1, v41
	v_cvt_f32_i32_e32 v40, v40
	v_cvt_f32_u32_e32 v42, v42
	v_exp_f32_e32 v44, v25
	v_add_u32_e32 v43, 2, v41
	v_mul_f32_e32 v25, v171, v40
	v_mul_f32_e32 v40, v170, v42
	v_sub_u32_e32 v42, 0x1fd, v41
	v_cvt_f32_i32_e32 v42, v42
	v_cvt_f32_u32_e32 v43, v43
	v_exp_f32_e32 v45, v40
	v_mov_b32_e32 v125, v67
	v_mul_f32_e32 v40, v171, v42
	v_sub_u32_e32 v42, 0x1fc, v41
	v_cvt_f32_i32_e32 v42, v42
	v_add_u32_e32 v41, 3, v41
	v_cvt_f32_u32_e32 v41, v41
	v_exp_f32_e32 v46, v40
	v_mul_f32_e32 v40, v170, v43
	v_exp_f32_e32 v48, v40
	v_mul_f32_e32 v40, v171, v42
	v_exp_f32_e32 v47, v40
	v_mul_f32_e32 v40, v170, v41
	v_exp_f32_e32 v49, v40
	v_ashrrev_i32_e32 v40, 10, v50
	v_and_b32_e32 v40, -4, v40
	v_add_u32_e32 v40, s44, v40
	v_ashrrev_i32_e32 v41, 31, v40
	v_lshlrev_b64 v[40:41], 22, v[40:41]
	v_lshlrev_b32_e32 v42, 10, v50
	v_lshl_add_u64 v[40:41], s[40:41], 0, v[40:41]
	v_and_b32_e32 v42, 0x380000, v42
	v_mov_b32_e32 v43, v67
	v_lshl_add_u64 v[40:41], v[40:41], 0, v[42:43]
	v_lshlrev_b32_e32 v42, 5, v50
	v_and_b32_e32 v42, 0x3f00, v42
	v_lshl_add_u64 v[40:41], v[40:41], 0, v[42:43]
	v_and_b32_e32 v42, 7, v50
	v_lshl_add_u64 v[40:41], v[40:41], 0, v[124:125]
	v_lshlrev_b32_e32 v42, 1, v42
	v_exp_f32_e32 v24, v24
	v_exp_f32_e32 v25, v25
	v_lshl_add_u64 v[50:51], v[40:41], 0, v[42:43]
	v_mfma_f32_16x16x32_bf16 v[40:43], v[20:23], v[2:5], 0
	s_lshl_b32 s72, s4, 1
	v_lshl_add_u64 v[50:51], v[50:51], 0, s[72:73]
	s_mov_b32 s7, 0x40000
	v_mfma_f32_16x16x32_bf16 v[20:23], v[20:23], v[6:9], 0
	s_nop 3
	v_mul_f32_e64 v52, v46, v42
	v_mul_f32_e64 v53, v47, v43
	v_pk_mul_f32 v[54:55], v[24:25], v[40:41]
	v_pk_mul_f32 v[42:43], v[48:49], v[42:43]
	v_pk_mul_f32 v[40:41], v[44:45], v[40:41]
	v_cvt_pk_bf16_f32 v54, v54, v55
	v_cvt_pk_bf16_f32 v55, v52, v53
	v_mov_b32_e32 v196, v54
	v_mov_b32_e32 v197, v55
	v_lshl_add_u64 v[200:201], v[50:51], 0, v[202:203]
	v_cvt_pk_bf16_f32 v40, v40, v41
	v_cvt_pk_bf16_f32 v41, v42, v43
	v_add_co_u32_e32 v42, vcc, s7, v50
	s_movk_i32 s7, 0x4000
	s_nop 0
	v_addc_co_u32_e32 v43, vcc, 0, v51, vcc
	v_mov_b32_e32 v198, v40
	v_mov_b32_e32 v199, v41
	s_nop 1
	v_permlane16_swap_b32_e32 v196, v198
	v_permlane16_swap_b32_e32 v197, v199
	global_store_dwordx4 v[200:201], v[196:199], off
	v_pk_mul_f32 v[40:41], v[46:47], v[22:23]
	v_pk_mul_f32 v[42:43], v[24:25], v[20:21]
	v_pk_mul_f32 v[22:23], v[48:49], v[22:23]
	v_cvt_pk_bf16_f32 v42, v42, v43
	v_cvt_pk_bf16_f32 v43, v40, v41
	v_add_co_u32_e32 v40, vcc, s7, v50
	v_pk_mul_f32 v[20:21], v[44:45], v[20:21]
	s_nop 0
	v_addc_co_u32_e32 v41, vcc, 0, v51, vcc
	s_mov_b32 s7, 0x44000
	v_cvt_pk_bf16_f32 v20, v20, v21
	v_cvt_pk_bf16_f32 v21, v22, v23
	v_add_co_u32_e32 v22, vcc, s7, v50
	v_mov_b32_e32 v228, v42
	v_mov_b32_e32 v229, v43
	v_lshl_add_u64 v[232:233], v[40:41], 0, v[202:203]
	s_nop 0
	v_addc_co_u32_e32 v23, vcc, 0, v51, vcc
	v_mov_b32_e32 v230, v20
	v_mov_b32_e32 v231, v21
	s_nop 1
	v_permlane16_swap_b32_e32 v228, v230
	v_permlane16_swap_b32_e32 v229, v231
	global_store_dwordx4 v[232:233], v[228:231], off
	v_mfma_f32_16x16x32_bf16 v[20:23], v[36:39], v[2:5], 0
	s_mov_b32 s7, 0x20000
	s_nop 6
	v_pk_mul_f32 v[40:41], v[46:47], v[22:23]
	v_pk_mul_f32 v[42:43], v[24:25], v[20:21]
	v_pk_mul_f32 v[22:23], v[48:49], v[22:23]
	v_cvt_pk_bf16_f32 v42, v42, v43
	v_cvt_pk_bf16_f32 v43, v40, v41
	v_add_co_u32_e32 v40, vcc, s7, v50
	v_pk_mul_f32 v[20:21], v[44:45], v[20:21]
	s_nop 0
	v_addc_co_u32_e32 v41, vcc, 0, v51, vcc
	s_mov_b32 s7, 0x60000
	v_cvt_pk_bf16_f32 v20, v20, v21
	v_cvt_pk_bf16_f32 v21, v22, v23
	v_add_co_u32_e32 v22, vcc, s7, v50
	s_mov_b32 s7, 0x24000
	s_nop 0
	v_addc_co_u32_e32 v23, vcc, 0, v51, vcc
	v_mov_b32_e32 v198, v20
	v_mov_b32_e32 v199, v21
	v_mfma_f32_16x16x32_bf16 v[20:23], v[36:39], v[6:9], 0
	v_mov_b32_e32 v196, v42
	v_mov_b32_e32 v197, v43
	v_lshl_add_u64 v[200:201], v[40:41], 0, v[202:203]
	s_nop 1
	v_permlane16_swap_b32_e32 v196, v198
	v_permlane16_swap_b32_e32 v197, v199
	global_store_dwordx4 v[200:201], v[196:199], off
	s_nop 6
	v_pk_mul_f32 v[36:37], v[46:47], v[22:23]
	v_pk_mul_f32 v[24:25], v[24:25], v[20:21]
	v_pk_mul_f32 v[22:23], v[48:49], v[22:23]
	v_cvt_pk_bf16_f32 v24, v24, v25
	v_cvt_pk_bf16_f32 v25, v36, v37
	v_add_co_u32_e32 v36, vcc, s7, v50
	v_pk_mul_f32 v[20:21], v[44:45], v[20:21]
	s_nop 0
	v_addc_co_u32_e32 v37, vcc, 0, v51, vcc
	v_cvt_pk_bf16_f32 v20, v20, v21
	v_cvt_pk_bf16_f32 v21, v22, v23
	v_add_co_u32_e32 v22, vcc, 0x64000, v50
	v_mov_b32_e32 v228, v24
	v_mov_b32_e32 v229, v25
	v_lshl_add_u64 v[232:233], v[36:37], 0, v[202:203]
	s_nop 0
	v_addc_co_u32_e32 v23, vcc, 0, v51, vcc
	v_mov_b32_e32 v230, v20
	v_mov_b32_e32 v231, v21
	s_nop 1
	v_permlane16_swap_b32_e32 v228, v230
	v_permlane16_swap_b32_e32 v229, v231
	global_store_dwordx4 v[232:233], v[228:231], off
	s_cbranch_execnz .LBB0_343
